# first K-loop trip peeled with srcC=0 in all six main GEMM phases; accumulator-clearing MFMAs removed
# speedup vs baseline: 1.0168x; 1.0096x over previous
; #define PG8_STAGE(bufoff, gbase, voff) do { PG8_GLDS((const char*)(gbase), (voff)[0], ldsb + (bufoff)); PG8_GLDS((const char*)(gbase), (voff)[1], ldsb + (bufoff) + 8192u); } while (0)
; #define PG8_STAGEA(bufoff, gbase, o0, o1) do { PG8_GLDS((const char*)(gbase), (o0), ldsb + (bufoff)); PG8_GLDS((const char*)(gbase), (o1), ldsb + (bufoff) + 8192u); } while (0)
; #define PG8_STAGEA1(bufoff, gbase) do { if constexpr (Sched::GATHER) { PG8_STAGEA(bufoff, gbase, vA2, vA3); } else { PG8_STAGEA(bufoff, (gbase) + hstep, vA0, vA1); } } while (0)
; #define PG8_WAIT_V(n) asm volatile("s_waitcnt vmcnt(" #n ")" ::: "memory")
; #define PG8_BAR __builtin_amdgcn_s_barrier()
; template <class Epi, class Sched, bool F8 = false, bool PF = false, bool I8 = false, int PID = -1>
; __device__ __forceinline__ void gemm_phase(LAS unsigned char* lds, LAS unsigned char* xlds, const int RP, const int RPB, const int nt, const Sched& S, const Epi& E, const int stagger_ticks) {
;     ...
;     const int tid = tid_, wid = __builtin_amdgcn_readfirstlane(tid >> 6), lane = tid & 63, wr = wid >> 2, wc = wid & 3, fr = lane & 15, fq = lane >> 4;
;     int Rr[2], Cc[2]; unsigned voffB[2];
; #pragma unroll
;     for (int i = 0; i < 2; ++i) { int R, C; stage_rc(tid * 16 + i * 8192, R, C); Rr[i] = R; Cc[i] = C; const int Rb = Epi::PERM ? permB(R) : R; voffB[i] = (unsigned)(Rb * RPB + C * 2); }
;     ...
;     PG8_ZERO_ACC();
;     PG8_STAGE(PG8_SB(0, 0), cB, voffB); PG8_STAGE(PG8_SB(0, 1), cB + hstepB, voffB); PG8_STAGEA(PG8_SA(0, 0), cA, vA0, vA1); PG8_STAGEA1(PG8_SA(0, 1), cA);
;     if (wr == 1) PG8_BAR;
;     PG8_WAIT_V(2); PG8_BAR;
;     PG8_STAGE(PG8_SB(1, 0), cB + kstep, voffB); PG8_STAGEA(PG8_SA(1, 0), cA + kstep, vA0, vA1); PG8_STAGE(PG8_SB(1, 1), cB + hstepB + kstep, voffB);
;     PG8_WAIT_V(6); PG8_BAR;
.LBB0_207:
	v_bfe_i32 v4, v46, 27, 1
	v_lshlrev_b32_e32 v2, 4, v46
	v_lshrrev_b32_e32 v4, 22, v4
	v_add_u32_e32 v4, v2, v4
	v_and_b32_e32 v4, 0xfffffc00, v4
	v_sub_u32_e32 v4, v2, v4
	v_lshrrev_b32_e32 v5, 4, v4
	v_bitop3_b32 v4, v5, v4, 32 bitop3:0x6c
	s_waitcnt vmcnt(6)
	v_ashrrev_i32_e32 v6, 31, v4
	v_ashrrev_i32_e32 v3, 31, v46
	v_lshrrev_b32_e32 v6, 26, v6
	v_lshrrev_b32_e32 v3, 26, v3
	v_add_u32_e32 v6, v4, v6
	v_add_u32_e32 v3, v46, v3
	v_ashrrev_i32_e32 v7, 6, v6
	v_and_b32_e32 v6, 0xc0, v6
	v_ashrrev_i32_e32 v3, 6, v3
	v_sub_u32_e32 v4, v4, v6
	v_mov_b32_e32 v6, 1
	v_lshlrev_b32_e32 v5, 3, v3
	v_lshlrev_b32_e32 v3, 5, v3
	v_ashrrev_i16_sdwa v4, v6, sext(v4) dst_sel:DWORD dst_unused:UNUSED_PAD src0_sel:DWORD src1_sel:BYTE_0
	v_and_b32_e32 v3, 32, v3
	v_bfe_i32 v4, v4, 0, 16
	v_add_u32_e32 v2, 0x2000, v2
	v_add_lshl_u32 v3, v3, v4, 1
	v_ashrrev_i32_e32 v4, 31, v2
	v_lshrrev_b32_e32 v4, 22, v4
	v_add_u32_e32 v4, v2, v4
	v_ashrrev_i32_e32 v4, 10, v4
	v_mul_i32_i24_e32 v8, 0x400, v4
	v_sub_u32_e32 v2, v2, v8
	v_lshrrev_b32_e32 v8, 4, v2
	v_bitop3_b32 v2, v8, v2, 32 bitop3:0x6c
	v_ashrrev_i32_e32 v9, 31, v2
	v_lshrrev_b32_e32 v9, 26, v9
	v_add_u32_e32 v9, v2, v9
	s_waitcnt vmcnt(5)
	v_ashrrev_i32_e32 v10, 6, v9
	v_and_b32_e32 v9, 0xc0, v9
	v_sub_u32_e32 v2, v2, v9
	v_and_b32_e32 v5, -16, v5
	v_lshlrev_b32_e32 v8, 3, v4
	v_lshlrev_b32_e32 v4, 5, v4
	v_ashrrev_i16_sdwa v2, v6, sext(v2) dst_sel:DWORD dst_unused:UNUSED_PAD src0_sel:DWORD src1_sel:BYTE_0
	v_add_u32_e32 v5, v7, v5
	v_and_b32_e32 v4, 32, v4
	v_bfe_i32 v2, v2, 0, 16
	v_add_lshl_u32 v2, v4, v2, 1
	v_lshl_add_u32 v180, v5, 10, v3
	v_lshlrev_b32_e32 v4, 1, v5
	v_lshlrev_b32_e32 v6, 2, v5
	v_lshrrev_b32_e32 v5, 2, v5
	v_and_b32_e32 v7, 3, v7
	v_and_b32_e32 v8, -16, v8
	v_and_b32_e32 v4, 0x3fffc0, v4
	v_and_b32_e32 v5, 4, v5
	v_and_or_b32 v6, v6, 48, v7
	v_add_u32_e32 v8, v10, v8
	v_or3_b32 v4, v6, v4, v5
	v_lshl_add_u32 v182, v4, 10, v3
	v_lshlrev_b32_e32 v3, 1, v8
	v_lshlrev_b32_e32 v4, 2, v8
	v_lshrrev_b32_e32 v5, 2, v8
	v_and_b32_e32 v6, 3, v10
	v_mov_b32_e32 v178, 0
	v_and_b32_e32 v3, 0x3fffc0, v3
	v_and_b32_e32 v5, 4, v5
	v_and_or_b32 v4, v4, 48, v6
	s_lshl_b32 s7, s46, 10
	v_mov_b32_e32 v179, v178
	v_or3_b32 v3, v4, v3, v5
	s_add_i32 s7, s7, 0
	v_mov_b64_e32 v[48:49], v[178:179]
	v_lshl_add_u32 v181, v8, 10, v2
	v_lshl_add_u32 v183, v3, 10, v2
	s_add_i32 s19, s7, 0x10000
	s_waitcnt vmcnt(0)
	s_ashr_i32 s8, s44, 8
	s_mov_b32 m0, s19
	s_nop 0
	global_load_lds_dwordx4 v182, s[12:13]
	s_add_i32 s19, s7, 0x12000
	s_mov_b32 m0, s19
	s_nop 0
	global_load_lds_dwordx4 v183, s[12:13]
	s_add_u32 s40, s12, 0x2000
	s_addc_u32 s41, s13, 0
	s_add_i32 s19, s7, 0x14000
	s_mov_b32 m0, s19
	s_nop 0
	global_load_lds_dwordx4 v182, s[40:41]
	s_add_i32 s19, s7, 0x16000
	s_mov_b32 m0, s19
	s_nop 0
	global_load_lds_dwordx4 v183, s[40:41]
	s_add_i32 s19, s7, 0x2000
	s_mov_b32 m0, s7
	s_nop 0
	global_load_lds_dwordx4 v180, s[10:11]
	s_add_u32 s48, s10, 0x20000
	s_mov_b32 m0, s19
	s_nop 0
	global_load_lds_dwordx4 v181, s[10:11]
	s_addc_u32 s49, s11, 0
	s_add_i32 s19, s7, 0x4000
	s_mov_b32 m0, s19
	s_nop 0
	global_load_lds_dwordx4 v180, s[48:49]
	s_add_i32 s19, s7, 0x6000
	s_mov_b32 m0, s19
	s_nop 0
	global_load_lds_dwordx4 v181, s[48:49]
	s_cmp_eq_u32 s8, 1
	s_cselect_b64 s[40:41], -1, 0
	s_cmp_lg_u32 s8, 1
	s_cbranch_scc1 .LBB0_209
	s_barrier

; #define PG8_STAGE(bufoff, gbase, voff) do { PG8_GLDS((const char*)(gbase), (voff)[0], ldsb + (bufoff)); PG8_GLDS((const char*)(gbase), (voff)[1], ldsb + (bufoff) + 8192u); } while (0)
; #define PG8_STAGEA(bufoff, gbase, o0, o1) do { PG8_GLDS((const char*)(gbase), (o0), ldsb + (bufoff)); PG8_GLDS((const char*)(gbase), (o1), ldsb + (bufoff) + 8192u); } while (0)
; #define PG8_STAGEA1(bufoff, gbase) do { if constexpr (Sched::GATHER) { PG8_STAGEA(bufoff, gbase, vA2, vA3); } else { PG8_STAGEA(bufoff, (gbase) + hstep, vA0, vA1); } } while (0)
; template <class Epi, class Sched, bool F8 = false, bool PF = false, bool I8 = false, int PID = -1>
; __device__ __forceinline__ void gemm_phase(LAS unsigned char* lds, LAS unsigned char* xlds, const int RP, const int RPB, const int nt, const Sched& S, const Epi& E, const int stagger_ticks) {
;     ...
;         for (int t = 0; t < nt; t += 2) {
;             const bool last = (t == nt - 2);
;             unsigned ldsb = ldsb0; asm volatile("" : "+s"(ldsb));
;             const char* a1 = cA + (size_t)(t + 1) * kstep;
;             const char* a2 = last ? nA : cA + (size_t)(t + 2) * kstep; const char* b2 = last ? nB : cB + (size_t)(t + 2) * kstep;
;             const char* a3 = a2 + kstep; const char* b3 = b2 + kstep;
;             if constexpr (PF) { const char* pfa = (t + 4 < nt) ? cA + (size_t)(t + 4) * kstep : nA + (size_t)(t + 4 - nt) * kstep;
;                 asm volatile("s_mov_b32 m0, %2\n\ts_nop 0\n\tglobal_load_lds_dword %0, %1" :: "v"(voffP), "s"(pfa), "s"(ldsP) : "memory", "m0"); }
;             const bool relax = (Epi::RELAX > 0) && (t == 0) && epi_ran;
;             PG8_LDB(B0, 0, 0); PG8_LDB(B1, 0, 1); PG8_SCHED; PG8_LDA(At, 0, 0); PG8_STAGEA1(PG8_SA(1, 1), a1);
;             if (Sched::GATHER) { if (last) { const u32x4 nv = *nslot; vA0 = nv.x; vA1 = nv.y; vA2 = nv.z; vA3 = nv.w; } }
;             PG8_WAIT_VX(); PG8_WAIT_L(0); PG8_BAR; PG8_MMA(0, 0, At, B0); PG8_MMA(0, 1, At, B1); PG8_BAR; PG8_SCHED;
;             if constexpr (Epi::BIAS_DMA) { if (t == 0 && has_next) E.bias_dma(nxt, xlds + 8192 + ((ui + 1) & 1) * Epi::BIAS_STRIDE, wid, lane); }
;             PG8_LDA(At, 0, 1); PG8_STAGE(PG8_SB(0, 0), b2, voffB); PG8_STAGE(PG8_SB(0, 1), b2 + hstepB, voffB); PG8_STAGEA(PG8_SA(0, 0), a2, vA0, vA1);
;             PG8_WAIT_VX(); PG8_WAIT_L(0); PG8_BAR; PG8_MMA(1, 0, At, B0); PG8_MMA(1, 1, At, B1); PG8_BAR; PG8_SCHED;
.Lmy_z1t:
	s_mov_b32 s82, s7
	v_add_u32_e32 v46, 0x10000, v184
	ds_read_b128 v[162:165], v46
	ds_read_b128 v[166:169], v46 offset:1024
	ds_read_b128 v[170:173], v46 offset:2048
	ds_read_b128 v[174:177], v46 offset:3072
	v_add_u32_e32 v46, 0x14000, v184
	ds_read_b128 v[146:149], v46
	ds_read_b128 v[150:153], v46 offset:1024
	ds_read_b128 v[154:157], v46 offset:2048
	ds_read_b128 v[158:161], v46 offset:3072
	ds_read_b128 v[186:189], v185
	ds_read_b128 v[190:193], v185 offset:1024
	ds_read_b128 v[194:197], v185 offset:2048
	ds_read_b128 v[198:201], v185 offset:3072
	ds_read_b128 v[202:205], v185 offset:4096
	ds_read_b128 v[206:209], v185 offset:5120
	ds_read_b128 v[210:213], v185 offset:6144
	ds_read_b128 v[214:217], v185 offset:7168
	s_add_i32 s48, s82, 0xc000
	s_mov_b32 m0, s48
	s_nop 0
	global_load_lds_dwordx4 v180, s[2:3]
	s_add_i32 s48, s82, 0xe000
	s_mov_b32 m0, s48
	s_nop 0
	global_load_lds_dwordx4 v181, s[2:3]
	s_waitcnt vmcnt(8)
	s_waitcnt lgkmcnt(0)
	s_barrier
	s_setprio 1
	s_waitcnt lgkmcnt(7)
	v_mfma_i32_16x16x64_i8 v[46:49], v[162:165], v[186:189], 0
	v_mfma_i32_16x16x64_i8 v[54:57], v[170:173], v[186:189], 0
	s_waitcnt lgkmcnt(5)
	v_mfma_i32_16x16x64_i8 v[58:61], v[162:165], v[194:197], 0
	v_mfma_i32_16x16x64_i8 v[66:69], v[170:173], v[194:197], 0
	s_waitcnt lgkmcnt(3)
	v_mfma_i32_16x16x64_i8 v[110:113], v[162:165], v[202:205], 0
	v_mfma_i32_16x16x64_i8 v[106:109], v[170:173], v[202:205], 0
	s_waitcnt lgkmcnt(1)
	v_mfma_i32_16x16x64_i8 v[94:97], v[162:165], v[210:213], 0
	v_mfma_i32_16x16x64_i8 v[90:93], v[170:173], v[210:213], 0
	v_mfma_i32_16x16x64_i8 v[46:49], v[166:169], v[190:193], v[46:49]
	v_mfma_i32_16x16x64_i8 v[54:57], v[174:177], v[190:193], v[54:57]
	v_mfma_i32_16x16x64_i8 v[58:61], v[166:169], v[198:201], v[58:61]
	v_mfma_i32_16x16x64_i8 v[66:69], v[174:177], v[198:201], v[66:69]
	v_mfma_i32_16x16x64_i8 v[110:113], v[166:169], v[206:209], v[110:113]
	v_mfma_i32_16x16x64_i8 v[106:109], v[174:177], v[206:209], v[106:109]
	s_waitcnt lgkmcnt(0)
	v_mfma_i32_16x16x64_i8 v[94:97], v[166:169], v[214:217], v[94:97]
	v_mfma_i32_16x16x64_i8 v[90:93], v[174:177], v[214:217], v[90:93]
	s_setprio 0
	s_setprio 1
	v_mfma_i32_16x16x64_i8 v[122:125], v[146:149], v[186:189], 0
	v_mfma_i32_16x16x64_i8 v[134:137], v[150:153], v[190:193], v[122:125]
	v_mfma_i32_16x16x64_i8 v[122:125], v[154:157], v[186:189], 0
	v_mfma_i32_16x16x64_i8 v[118:121], v[146:149], v[194:197], 0
	v_mfma_i32_16x16x64_i8 v[114:117], v[154:157], v[194:197], 0
	v_mfma_i32_16x16x64_i8 v[102:105], v[146:149], v[202:205], 0
	v_mfma_i32_16x16x64_i8 v[98:101], v[154:157], v[202:205], 0
	v_mfma_i32_16x16x64_i8 v[86:89], v[146:149], v[210:213], 0
	v_mfma_i32_16x16x64_i8 v[82:85], v[154:157], v[210:213], 0
	v_mfma_i32_16x16x64_i8 v[130:133], v[158:161], v[190:193], v[122:125]
	v_mfma_i32_16x16x64_i8 v[118:121], v[150:153], v[198:201], v[118:121]
	v_mfma_i32_16x16x64_i8 v[114:117], v[158:161], v[198:201], v[114:117]
	v_mfma_i32_16x16x64_i8 v[102:105], v[150:153], v[206:209], v[102:105]
	v_mfma_i32_16x16x64_i8 v[98:101], v[158:161], v[206:209], v[98:101]
	v_mfma_i32_16x16x64_i8 v[86:89], v[150:153], v[214:217], v[86:89]
	v_mfma_i32_16x16x64_i8 v[82:85], v[158:161], v[214:217], v[82:85]
	s_setprio 0
	s_barrier
	s_cmp_lg_u32 s79, -2
	s_cselect_b64 s[48:49], -1, 0
	s_or_b64 s[48:49], s[46:47], s[48:49]
	s_and_b64 vcc, exec, s[48:49]
	s_cbranch_vccnz .Lmy_z1b
	s_mov_b32 m0, s78
	s_nop 0
	global_load_lds_dword v1, s[0:1]
	s_branch .Lmy_z1b
.Lmy_z1b:
	s_add_u32 s48, s2, 0xfffe0080
	s_addc_u32 s49, s3, -1
	s_cmp_eq_u32 s79, 4
	s_cselect_b32 s62, s10, s48
	s_cselect_b32 s63, s11, s49
	s_cselect_b32 s50, s12, s76
	s_cselect_b32 s51, s13, s77
	s_add_u32 s48, s62, 0x80
	s_addc_u32 s49, s63, 0
	s_add_u32 s60, s50, 0x80
	s_addc_u32 s61, s51, 0
	ds_read_b128 v[122:125], v185 offset:16384
	ds_read_b128 v[126:129], v185 offset:17408
	ds_read_b128 v[138:141], v185 offset:18432
	ds_read_b128 v[142:145], v185 offset:19456
	ds_read_b128 v[186:189], v185 offset:20480
	ds_read_b128 v[190:193], v185 offset:21504
	ds_read_b128 v[194:197], v185 offset:22528
	ds_read_b128 v[198:201], v185 offset:23552
	s_add_i32 s83, s82, 0x10000
	s_mov_b32 m0, s83
	s_nop 0
	global_load_lds_dwordx4 v182, s[50:51]
	s_add_i32 s83, s82, 0x12000
	s_mov_b32 m0, s83
	s_nop 0
	global_load_lds_dwordx4 v183, s[50:51]
	s_add_u32 s86, s50, 0x2000
	s_addc_u32 s87, s51, 0
	s_add_i32 s83, s82, 0x14000
	s_mov_b32 m0, s83
	s_nop 0
	global_load_lds_dwordx4 v182, s[86:87]
	s_add_i32 s83, s82, 0x16000
	s_mov_b32 m0, s83
	s_nop 0
	global_load_lds_dwordx4 v183, s[86:87]
	s_add_i32 s83, s82, 0x2000
	s_mov_b32 m0, s82
	s_nop 0
	global_load_lds_dwordx4 v180, s[62:63]
	s_nop 0
	s_mov_b32 m0, s83
	s_nop 0
	global_load_lds_dwordx4 v181, s[62:63]
	s_waitcnt vmcnt(8)
	s_waitcnt lgkmcnt(0)
	s_barrier
; #define PG8_STAGE(bufoff, gbase, voff) do { PG8_GLDS((const char*)(gbase), (voff)[0], ldsb + (bufoff)); PG8_GLDS((const char*)(gbase), (voff)[1], ldsb + (bufoff) + 8192u); } while (0)
; #define PG8_STAGEA(bufoff, gbase, o0, o1) do { PG8_GLDS((const char*)(gbase), (o0), ldsb + (bufoff)); PG8_GLDS((const char*)(gbase), (o1), ldsb + (bufoff) + 8192u); } while (0)
; #define PG8_STAGEA1(bufoff, gbase) do { if constexpr (Sched::GATHER) { PG8_STAGEA(bufoff, gbase, vA2, vA3); } else { PG8_STAGEA(bufoff, (gbase) + hstep, vA0, vA1); } } while (0)
; #define PG8_LDA(dst, b, h) do { if constexpr (F8) { _Pragma("unroll") for (int m = 0; m < 4; ++m) dst##8[m] = PG8_LD32(lds + PG8_SA(b, h) + aoff + m * 2048); } else { \
;         _Pragma("unroll") for (int m = 0; m < 4; ++m) _Pragma("unroll") for (int k = 0; k < 2; ++k) dst[m][k] = *(const LAS bf16x8*)(lds + PG8_SA(b, h) + aoff + m * 2048 + k * 1024); } } while (0)
; #define PG8_WAIT_VR() PG8_WAIT_V(8)
; #define PG8_WAIT_L(n) asm volatile("s_waitcnt lgkmcnt(" #n ")" ::: "memory")
; template <class Epi, class Sched, bool F8 = false, bool PF = false, bool I8 = false, int PID = -1>
; __device__ __forceinline__ void gemm_phase(LAS unsigned char* lds, LAS unsigned char* xlds, const int RP, const int RPB, const int nt, const Sched& S, const Epi& E, const int stagger_ticks) {
;     ...
;             PG8_WAIT_VX(); PG8_WAIT_L(0); PG8_BAR; PG8_MMA(0, 0, At, B0); PG8_MMA(0, 1, At, B1); PG8_BAR; PG8_SCHED;
;             if constexpr (Epi::BIAS_DMA) { if (t == 0 && has_next) E.bias_dma(nxt, xlds + 8192 + ((ui + 1) & 1) * Epi::BIAS_STRIDE, wid, lane); }
;             PG8_LDA(At, 0, 1); PG8_STAGE(PG8_SB(0, 0), b2, voffB); PG8_STAGE(PG8_SB(0, 1), b2 + hstepB, voffB); PG8_STAGEA(PG8_SA(0, 0), a2, vA0, vA1);
;             PG8_WAIT_VX(); PG8_WAIT_L(0); PG8_BAR; PG8_MMA(1, 0, At, B0); PG8_MMA(1, 1, At, B1); PG8_BAR; PG8_SCHED;
;             PG8_LDB(B0, 1, 0); PG8_LDB(B1, 1, 1); PG8_SCHED; PG8_LDA(At, 1, 0); PG8_STAGEA1(PG8_SA(0, 1), a2);
;             PG8_WAIT_VR(); PG8_WAIT_L(0); PG8_BAR; PG8_MMA(0, 0, At, B0); PG8_MMA(0, 1, At, B1); PG8_BAR; PG8_SCHED;
;             PG8_LDA(At, 1, 1); PG8_STAGE(PG8_SB(1, 0), b3, voffB); PG8_STAGE(PG8_SB(1, 1), b3 + hstepB, voffB); PG8_STAGEA(PG8_SA(1, 0), a3, vA0, vA1);
;             PG8_WAIT_VR(); PG8_WAIT_L(0); PG8_BAR; PG8_MMA(1, 0, At, B0); PG8_MMA(1, 1, At, B1); PG8_BAR; PG8_SCHED;
	s_setprio 1
	s_waitcnt lgkmcnt(7)
	v_mfma_i32_16x16x64_i8 v[78:81], v[162:165], v[122:125], 0
	v_mfma_i32_16x16x64_i8 v[74:77], v[170:173], v[122:125], 0
	s_waitcnt lgkmcnt(5)
	v_mfma_i32_16x16x64_i8 v[50:53], v[162:165], v[138:141], 0
	v_mfma_i32_16x16x64_i8 v[42:45], v[170:173], v[138:141], 0
	s_waitcnt lgkmcnt(3)
	v_mfma_i32_16x16x64_i8 v[30:33], v[162:165], v[186:189], 0
	v_mfma_i32_16x16x64_i8 v[26:29], v[170:173], v[186:189], 0
	s_waitcnt lgkmcnt(1)
	v_mfma_i32_16x16x64_i8 v[14:17], v[162:165], v[194:197], 0
	v_mfma_i32_16x16x64_i8 v[10:13], v[170:173], v[194:197], 0
	v_mfma_i32_16x16x64_i8 v[78:81], v[166:169], v[126:129], v[78:81]
	v_mfma_i32_16x16x64_i8 v[74:77], v[174:177], v[126:129], v[74:77]
	v_mfma_i32_16x16x64_i8 v[50:53], v[166:169], v[142:145], v[50:53]
	v_mfma_i32_16x16x64_i8 v[42:45], v[174:177], v[142:145], v[42:45]
	v_mfma_i32_16x16x64_i8 v[30:33], v[166:169], v[190:193], v[30:33]
	v_mfma_i32_16x16x64_i8 v[26:29], v[174:177], v[190:193], v[26:29]
	s_waitcnt lgkmcnt(0)
	v_mfma_i32_16x16x64_i8 v[14:17], v[166:169], v[198:201], v[14:17]
	v_mfma_i32_16x16x64_i8 v[10:13], v[174:177], v[198:201], v[10:13]
	s_setprio 0
	s_setprio 1
	v_mfma_i32_16x16x64_i8 v[70:73], v[146:149], v[122:125], 0
	v_mfma_i32_16x16x64_i8 v[62:65], v[154:157], v[122:125], 0
	v_mfma_i32_16x16x64_i8 v[38:41], v[146:149], v[138:141], 0
	v_mfma_i32_16x16x64_i8 v[34:37], v[154:157], v[138:141], 0
	v_mfma_i32_16x16x64_i8 v[22:25], v[146:149], v[186:189], 0
	v_mfma_i32_16x16x64_i8 v[18:21], v[154:157], v[186:189], 0
	v_mfma_i32_16x16x64_i8 v[6:9], v[146:149], v[194:197], 0
	v_mfma_i32_16x16x64_i8 v[2:5], v[154:157], v[194:197], 0
	v_mfma_i32_16x16x64_i8 v[70:73], v[150:153], v[126:129], v[70:73]
	v_mfma_i32_16x16x64_i8 v[62:65], v[158:161], v[126:129], v[62:65]
	v_mfma_i32_16x16x64_i8 v[38:41], v[150:153], v[142:145], v[38:41]
	v_mfma_i32_16x16x64_i8 v[34:37], v[158:161], v[142:145], v[34:37]
	v_mfma_i32_16x16x64_i8 v[22:25], v[150:153], v[190:193], v[22:25]
	v_mfma_i32_16x16x64_i8 v[18:21], v[158:161], v[190:193], v[18:21]
	v_mfma_i32_16x16x64_i8 v[6:9], v[150:153], v[198:201], v[6:9]
	v_mfma_i32_16x16x64_i8 v[2:5], v[158:161], v[198:201], v[2:5]
	s_setprio 0
	s_barrier
	v_add_u32_e32 v122, 0x18000, v184
	ds_read_b128 v[146:149], v122
	ds_read_b128 v[150:153], v122 offset:1024
	ds_read_b128 v[154:157], v122 offset:2048
	ds_read_b128 v[158:161], v122 offset:3072
	v_add_u32_e32 v122, 0x1c000, v184
	ds_read_b128 v[162:165], v122
	ds_read_b128 v[166:169], v122 offset:1024
	ds_read_b128 v[170:173], v122 offset:2048
	ds_read_b128 v[174:177], v122 offset:3072
	ds_read_b128 v[186:189], v185 offset:32768
	ds_read_b128 v[190:193], v185 offset:33792
	ds_read_b128 v[194:197], v185 offset:34816
	ds_read_b128 v[198:201], v185 offset:35840
	ds_read_b128 v[202:205], v185 offset:36864
	ds_read_b128 v[206:209], v185 offset:37888
	ds_read_b128 v[210:213], v185 offset:38912
	ds_read_b128 v[214:217], v185 offset:39936
	s_add_u32 s62, s62, 0x20000
	s_addc_u32 s63, s63, 0
	s_add_i32 s83, s82, 0x4000
	s_mov_b32 m0, s83
	s_nop 0
	global_load_lds_dwordx4 v180, s[62:63]
	s_add_i32 s83, s82, 0x6000
	s_mov_b32 m0, s83
	s_nop 0
	global_load_lds_dwordx4 v181, s[62:63]
	s_waitcnt vmcnt(8)
	s_waitcnt lgkmcnt(0)
	s_barrier
	s_setprio 1
	s_waitcnt lgkmcnt(7)
	v_mfma_i32_16x16x64_i8 v[46:49], v[146:149], v[186:189], v[46:49]
	s_waitcnt lgkmcnt(6)
	v_mfma_i32_16x16x64_i8 v[142:145], v[150:153], v[190:193], v[46:49]
	v_mfma_i32_16x16x64_i8 v[46:49], v[154:157], v[186:189], v[54:57]
	v_mfma_i32_16x16x64_i8 v[138:141], v[158:161], v[190:193], v[46:49]
	s_waitcnt lgkmcnt(5)
	v_mfma_i32_16x16x64_i8 v[46:49], v[146:149], v[194:197], v[58:61]
	s_waitcnt lgkmcnt(4)
	v_mfma_i32_16x16x64_i8 v[126:129], v[150:153], v[198:201], v[46:49]
	v_mfma_i32_16x16x64_i8 v[46:49], v[154:157], v[194:197], v[66:69]
	v_mfma_i32_16x16x64_i8 v[122:125], v[158:161], v[198:201], v[46:49]
	s_waitcnt lgkmcnt(3)
	v_mfma_i32_16x16x64_i8 v[46:49], v[146:149], v[202:205], v[110:113]
	s_waitcnt lgkmcnt(2)
	v_mfma_i32_16x16x64_i8 v[110:113], v[150:153], v[206:209], v[46:49]
	v_mfma_i32_16x16x64_i8 v[46:49], v[154:157], v[202:205], v[106:109]
	v_mfma_i32_16x16x64_i8 v[106:109], v[158:161], v[206:209], v[46:49]
	s_waitcnt lgkmcnt(1)
	v_mfma_i32_16x16x64_i8 v[46:49], v[146:149], v[210:213], v[94:97]
	s_waitcnt lgkmcnt(0)
	v_mfma_i32_16x16x64_i8 v[94:97], v[150:153], v[214:217], v[46:49]
	v_mfma_i32_16x16x64_i8 v[46:49], v[154:157], v[210:213], v[90:93]
	v_mfma_i32_16x16x64_i8 v[90:93], v[158:161], v[214:217], v[46:49]
	s_setprio 0
	s_setprio 1
	v_mfma_i32_16x16x64_i8 v[46:49], v[162:165], v[186:189], v[134:137]
	v_mfma_i32_16x16x64_i8 v[134:137], v[166:169], v[190:193], v[46:49]
	v_mfma_i32_16x16x64_i8 v[46:49], v[170:173], v[186:189], v[130:133]
	v_mfma_i32_16x16x64_i8 v[130:133], v[174:177], v[190:193], v[46:49]
	v_mfma_i32_16x16x64_i8 v[46:49], v[162:165], v[194:197], v[118:121]
	v_mfma_i32_16x16x64_i8 v[118:121], v[166:169], v[198:201], v[46:49]
	v_mfma_i32_16x16x64_i8 v[46:49], v[170:173], v[194:197], v[114:117]
	v_mfma_i32_16x16x64_i8 v[114:117], v[174:177], v[198:201], v[46:49]
	v_mfma_i32_16x16x64_i8 v[46:49], v[162:165], v[202:205], v[102:105]
	v_mfma_i32_16x16x64_i8 v[102:105], v[166:169], v[206:209], v[46:49]
	v_mfma_i32_16x16x64_i8 v[46:49], v[170:173], v[202:205], v[98:101]
	v_mfma_i32_16x16x64_i8 v[98:101], v[174:177], v[206:209], v[46:49]
	v_mfma_i32_16x16x64_i8 v[46:49], v[162:165], v[210:213], v[86:89]
	v_mfma_i32_16x16x64_i8 v[86:89], v[166:169], v[214:217], v[46:49]
	v_mfma_i32_16x16x64_i8 v[46:49], v[170:173], v[210:213], v[82:85]
	v_mfma_i32_16x16x64_i8 v[82:85], v[174:177], v[214:217], v[46:49]
	s_setprio 0
	s_barrier
; #define PG8_STAGE(bufoff, gbase, voff) do { PG8_GLDS((const char*)(gbase), (voff)[0], ldsb + (bufoff)); PG8_GLDS((const char*)(gbase), (voff)[1], ldsb + (bufoff) + 8192u); } while (0)
; #define PG8_STAGEA(bufoff, gbase, o0, o1) do { PG8_GLDS((const char*)(gbase), (o0), ldsb + (bufoff)); PG8_GLDS((const char*)(gbase), (o1), ldsb + (bufoff) + 8192u); } while (0)
; #define PG8_LDA(dst, b, h) do { if constexpr (F8) { _Pragma("unroll") for (int m = 0; m < 4; ++m) dst##8[m] = PG8_LD32(lds + PG8_SA(b, h) + aoff + m * 2048); } else { \
;         _Pragma("unroll") for (int m = 0; m < 4; ++m) _Pragma("unroll") for (int k = 0; k < 2; ++k) dst[m][k] = *(const LAS bf16x8*)(lds + PG8_SA(b, h) + aoff + m * 2048 + k * 1024); } } while (0)
; #define PG8_WAIT_VR() PG8_WAIT_V(8)
; #define PG8_WAIT_L(n) asm volatile("s_waitcnt lgkmcnt(" #n ")" ::: "memory")
; #define PG8_BAR __builtin_amdgcn_s_barrier()
; #define PG8_SCHED __builtin_amdgcn_sched_barrier(0)
; template <class Epi, class Sched, bool F8 = false, bool PF = false, bool I8 = false, int PID = -1>
; __device__ __forceinline__ void gemm_phase(LAS unsigned char* lds, LAS unsigned char* xlds, const int RP, const int RPB, const int nt, const Sched& S, const Epi& E, const int stagger_ticks) {
;     ...
;             PG8_WAIT_VR(); PG8_WAIT_L(0); PG8_BAR; PG8_MMA(0, 0, At, B0); PG8_MMA(0, 1, At, B1); PG8_BAR; PG8_SCHED;
;             PG8_LDA(At, 1, 1); PG8_STAGE(PG8_SB(1, 0), b3, voffB); PG8_STAGE(PG8_SB(1, 1), b3 + hstepB, voffB); PG8_STAGEA(PG8_SA(1, 0), a3, vA0, vA1);
;             PG8_WAIT_VR(); PG8_WAIT_L(0); PG8_BAR; PG8_MMA(1, 0, At, B0); PG8_MMA(1, 1, At, B1); PG8_BAR; PG8_SCHED;
;         }
	s_nop 4
	ds_read_b128 v[46:49], v185 offset:49152
	ds_read_b128 v[54:57], v185 offset:50176
	ds_read_b128 v[58:61], v185 offset:51200
	ds_read_b128 v[66:69], v185 offset:52224
	ds_read_b128 v[186:189], v185 offset:53248
	ds_read_b128 v[190:193], v185 offset:54272
	ds_read_b128 v[194:197], v185 offset:55296
	ds_read_b128 v[198:201], v185 offset:56320
	s_add_i32 s62, s82, 0x18000
	s_mov_b32 m0, s62
	s_nop 0
	global_load_lds_dwordx4 v182, s[60:61]
	s_add_i32 s62, s82, 0x1a000
	s_mov_b32 m0, s62
	s_nop 0
	global_load_lds_dwordx4 v183, s[60:61]
	s_add_u32 s50, s50, 0x2080
	s_addc_u32 s51, s51, 0
	s_add_i32 s60, s82, 0x1c000
	s_mov_b32 m0, s60
	s_nop 0
	global_load_lds_dwordx4 v182, s[50:51]
	s_add_i32 s60, s82, 0x1e000
	s_mov_b32 m0, s60
	s_nop 0
	global_load_lds_dwordx4 v183, s[50:51]
	s_add_i32 s50, s82, 0x8000
	s_mov_b32 m0, s50
	s_nop 0
	global_load_lds_dwordx4 v180, s[48:49]
	s_add_i32 s82, s82, 0xa000
	s_mov_b32 m0, s82
	s_nop 0
	global_load_lds_dwordx4 v181, s[48:49]
	s_waitcnt vmcnt(8)
	s_waitcnt lgkmcnt(0)
	s_barrier
	s_setprio 1
	s_waitcnt lgkmcnt(7)
	v_mfma_i32_16x16x64_i8 v[78:81], v[146:149], v[46:49], v[78:81]
	v_mfma_i32_16x16x64_i8 v[74:77], v[154:157], v[46:49], v[74:77]
	s_waitcnt lgkmcnt(5)
	v_mfma_i32_16x16x64_i8 v[50:53], v[146:149], v[58:61], v[50:53]
	v_mfma_i32_16x16x64_i8 v[42:45], v[154:157], v[58:61], v[42:45]
	s_waitcnt lgkmcnt(3)
	v_mfma_i32_16x16x64_i8 v[30:33], v[146:149], v[186:189], v[30:33]
	v_mfma_i32_16x16x64_i8 v[26:29], v[154:157], v[186:189], v[26:29]
	s_waitcnt lgkmcnt(1)
	v_mfma_i32_16x16x64_i8 v[14:17], v[146:149], v[194:197], v[14:17]
	v_mfma_i32_16x16x64_i8 v[10:13], v[154:157], v[194:197], v[10:13]
	v_mfma_i32_16x16x64_i8 v[78:81], v[150:153], v[54:57], v[78:81]
	v_mfma_i32_16x16x64_i8 v[74:77], v[158:161], v[54:57], v[74:77]
	v_mfma_i32_16x16x64_i8 v[50:53], v[150:153], v[66:69], v[50:53]
	v_mfma_i32_16x16x64_i8 v[42:45], v[158:161], v[66:69], v[42:45]
	v_mfma_i32_16x16x64_i8 v[30:33], v[150:153], v[190:193], v[30:33]
	v_mfma_i32_16x16x64_i8 v[26:29], v[158:161], v[190:193], v[26:29]
	s_waitcnt lgkmcnt(0)
	v_mfma_i32_16x16x64_i8 v[14:17], v[150:153], v[198:201], v[14:17]
	v_mfma_i32_16x16x64_i8 v[10:13], v[158:161], v[198:201], v[10:13]
	s_setprio 0
	s_setprio 1
	v_mfma_i32_16x16x64_i8 v[70:73], v[162:165], v[46:49], v[70:73]
	v_mfma_i32_16x16x64_i8 v[46:49], v[170:173], v[46:49], v[62:65]
	v_mfma_i32_16x16x64_i8 v[38:41], v[162:165], v[58:61], v[38:41]
	v_mfma_i32_16x16x64_i8 v[34:37], v[170:173], v[58:61], v[34:37]
	v_mfma_i32_16x16x64_i8 v[22:25], v[162:165], v[186:189], v[22:25]
	v_mfma_i32_16x16x64_i8 v[18:21], v[170:173], v[186:189], v[18:21]
	v_mfma_i32_16x16x64_i8 v[6:9], v[162:165], v[194:197], v[6:9]
	v_mfma_i32_16x16x64_i8 v[2:5], v[170:173], v[194:197], v[2:5]
	v_mfma_i32_16x16x64_i8 v[70:73], v[166:169], v[54:57], v[70:73]
	v_mfma_i32_16x16x64_i8 v[62:65], v[174:177], v[54:57], v[46:49]
	v_mfma_i32_16x16x64_i8 v[38:41], v[166:169], v[66:69], v[38:41]
	v_mfma_i32_16x16x64_i8 v[34:37], v[174:177], v[66:69], v[34:37]
	v_mfma_i32_16x16x64_i8 v[22:25], v[166:169], v[190:193], v[22:25]
	v_mfma_i32_16x16x64_i8 v[18:21], v[174:177], v[190:193], v[18:21]
	v_mfma_i32_16x16x64_i8 v[6:9], v[166:169], v[198:201], v[6:9]
	v_mfma_i32_16x16x64_i8 v[2:5], v[174:177], v[198:201], v[2:5]
	s_setprio 0
	s_barrier
	s_add_i32 s79, s79, 2
	s_add_u32 s76, s76, 0x100
	s_addc_u32 s77, s77, 0
	s_add_u32 s2, s2, 0x100
	s_addc_u32 s3, s3, 0
	s_cmp_gt_u32 s79, 5
	s_branch .LBB0_214

; #define PG8_BAR __builtin_amdgcn_s_barrier()
; template <class Epi, class Sched, bool F8 = false, bool PF = false, bool I8 = false, int PID = -1>
; __device__ __forceinline__ void gemm_phase(LAS unsigned char* lds, LAS unsigned char* xlds, const int RP, const int RPB, const int nt, const Sched& S, const Epi& E, const int stagger_ticks) {
;     ...
;         if (Sched::GATHER) { *nslot = (u32x4){gv[0], gv[1], gv[2], gv[3]}; asm volatile("" ::: "memory"); }
;         PG8_ZERO_ACC();
;         if (wr == 1) PG8_BAR;
.LBB0_261:
	v_mov_b32_e32 v179, v178
	v_mov_b64_e32 v[46:47], v[178:179]
	s_andn2_b64 vcc, exec, s[40:41]
	s_cbranch_vccnz .LBB0_210
	s_barrier
	s_branch .LBB0_210

; #define PG8_STAGE(bufoff, gbase, voff) do { PG8_GLDS((const char*)(gbase), (voff)[0], ldsb + (bufoff)); PG8_GLDS((const char*)(gbase), (voff)[1], ldsb + (bufoff) + 8192u); } while (0)
; #define PG8_STAGEA(bufoff, gbase, o0, o1) do { PG8_GLDS((const char*)(gbase), (o0), ldsb + (bufoff)); PG8_GLDS((const char*)(gbase), (o1), ldsb + (bufoff) + 8192u); } while (0)
; #define PG8_STAGEA1(bufoff, gbase) do { if constexpr (Sched::GATHER) { PG8_STAGEA(bufoff, gbase, vA2, vA3); } else { PG8_STAGEA(bufoff, (gbase) + hstep, vA0, vA1); } } while (0)
; #define PG8_WAIT_V(n) asm volatile("s_waitcnt vmcnt(" #n ")" ::: "memory")
; #define PG8_BAR __builtin_amdgcn_s_barrier()
; template <class Epi, class Sched, bool F8 = false, bool PF = false, bool I8 = false, int PID = -1>
; __device__ __forceinline__ void gemm_phase(LAS unsigned char* lds, LAS unsigned char* xlds, const int RP, const int RPB, const int nt, const Sched& S, const Epi& E, const int stagger_ticks) {
;     ...
;     const int tid = tid_, wid = __builtin_amdgcn_readfirstlane(tid >> 6), lane = tid & 63, wr = wid >> 2, wc = wid & 3, fr = lane & 15, fq = lane >> 4;
;     int Rr[2], Cc[2]; unsigned voffB[2];
; #pragma unroll
;     for (int i = 0; i < 2; ++i) { int R, C; stage_rc(tid * 16 + i * 8192, R, C); Rr[i] = R; Cc[i] = C; const int Rb = Epi::PERM ? permB(R) : R; voffB[i] = (unsigned)(Rb * RPB + C * 2); }
;     ...
;     PG8_ZERO_ACC();
;     PG8_STAGE(PG8_SB(0, 0), cB, voffB); PG8_STAGE(PG8_SB(0, 1), cB + hstepB, voffB); PG8_STAGEA(PG8_SA(0, 0), cA, vA0, vA1); PG8_STAGEA1(PG8_SA(0, 1), cA);
;     if (wr == 1) PG8_BAR;
;     PG8_WAIT_V(2); PG8_BAR;
;     PG8_STAGE(PG8_SB(1, 0), cB + kstep, voffB); PG8_STAGEA(PG8_SA(1, 0), cA + kstep, vA0, vA1); PG8_STAGE(PG8_SB(1, 1), cB + hstepB + kstep, voffB);
;     PG8_WAIT_V(6); PG8_BAR;
.LBB0_541:
	v_bfe_i32 v3, v130, 27, 1
	v_lshlrev_b32_e32 v1, 4, v130
	v_lshrrev_b32_e32 v3, 22, v3
	v_add_u32_e32 v3, v1, v3
	v_and_b32_e32 v3, 0xfffffc00, v3
	v_sub_u32_e32 v3, v1, v3
	v_lshrrev_b32_e32 v4, 4, v3
	v_bitop3_b32 v3, v4, v3, 32 bitop3:0x6c
	v_ashrrev_i32_e32 v5, 31, v3
	v_ashrrev_i32_e32 v2, 31, v130
	v_lshrrev_b32_e32 v5, 26, v5
	v_lshrrev_b32_e32 v2, 26, v2
	v_add_u32_e32 v5, v3, v5
	v_add_u32_e32 v2, v130, v2
	s_waitcnt vmcnt(6)
	v_ashrrev_i32_e32 v6, 6, v5
	v_and_b32_e32 v5, 0xc0, v5
	v_ashrrev_i32_e32 v2, 6, v2
	v_sub_u32_e32 v3, v3, v5
	v_mov_b32_e32 v5, 1
	v_lshlrev_b32_e32 v4, 3, v2
	v_lshlrev_b32_e32 v2, 5, v2
	v_ashrrev_i16_sdwa v3, v5, sext(v3) dst_sel:DWORD dst_unused:UNUSED_PAD src0_sel:DWORD src1_sel:BYTE_0
	v_and_b32_e32 v2, 32, v2
	v_bfe_i32 v3, v3, 0, 16
	v_add_u32_e32 v1, 0x2000, v1
	v_add_lshl_u32 v2, v2, v3, 1
	v_ashrrev_i32_e32 v3, 31, v1
	v_lshrrev_b32_e32 v3, 22, v3
	v_add_u32_e32 v3, v1, v3
	v_ashrrev_i32_e32 v3, 10, v3
	v_mul_i32_i24_e32 v7, 0x400, v3
	v_sub_u32_e32 v1, v1, v7
	v_lshrrev_b32_e32 v7, 4, v1
	v_bitop3_b32 v1, v7, v1, 32 bitop3:0x6c
	v_ashrrev_i32_e32 v8, 31, v1
	v_lshrrev_b32_e32 v8, 26, v8
	v_add_u32_e32 v8, v1, v8
	v_ashrrev_i32_e32 v9, 6, v8
	v_and_b32_e32 v8, 0xc0, v8
	v_sub_u32_e32 v1, v1, v8
	v_and_b32_e32 v4, -16, v4
	v_lshlrev_b32_e32 v7, 3, v3
	v_lshlrev_b32_e32 v3, 5, v3
	v_ashrrev_i16_sdwa v1, v5, sext(v1) dst_sel:DWORD dst_unused:UNUSED_PAD src0_sel:DWORD src1_sel:BYTE_0
	v_add_u32_e32 v4, v6, v4
	v_and_b32_e32 v3, 32, v3
	v_bfe_i32 v1, v1, 0, 16
	v_add_lshl_u32 v3, v3, v1, 1
	v_lshl_add_u32 v1, v4, 11, v2
	v_lshlrev_b32_e32 v5, 1, v4
	v_lshlrev_b32_e32 v8, 2, v4
	v_lshrrev_b32_e32 v4, 2, v4
	v_and_b32_e32 v6, 3, v6
	v_and_b32_e32 v7, -16, v7
	v_and_b32_e32 v5, 0x1fffc0, v5
	v_and_b32_e32 v4, 4, v4
	v_and_or_b32 v6, v8, 48, v6
	v_add_u32_e32 v7, v9, v7
	v_or3_b32 v4, v6, v5, v4
	s_ashr_i32 s7, s20, 6
	v_lshl_add_u32 v193, v4, 11, v2
	v_lshlrev_b32_e32 v2, 1, v7
	v_lshlrev_b32_e32 v4, 2, v7
	v_lshrrev_b32_e32 v5, 2, v7
	v_and_b32_e32 v6, 3, v9
	v_mov_b32_e32 v178, 0
	v_and_b32_e32 v2, 0x1fffc0, v2
	v_and_b32_e32 v5, 4, v5
	v_and_or_b32 v4, v4, 48, v6
	s_lshl_b32 s5, s7, 10
	v_mov_b32_e32 v179, v178
	v_or3_b32 v2, v4, v2, v5
	s_add_i32 s5, s5, 0
	v_mov_b64_e32 v[132:133], v[178:179]
	v_lshl_add_u32 v192, v7, 11, v3
	v_lshl_add_u32 v194, v2, 11, v3
	s_add_i32 s19, s5, 0x10000
	s_waitcnt vmcnt(0)
	s_ashr_i32 s15, s20, 8
	s_mov_b32 m0, s19
	s_nop 0
	global_load_lds_dwordx4 v193, s[10:11]
	s_add_i32 s19, s5, 0x12000
	s_mov_b32 m0, s19
	s_nop 0
	global_load_lds_dwordx4 v194, s[10:11]
	s_add_u32 s22, s10, 0x4000
	s_addc_u32 s23, s11, 0
	s_add_i32 s19, s5, 0x14000
	s_mov_b32 m0, s19
	s_nop 0
	global_load_lds_dwordx4 v193, s[22:23]
	s_add_i32 s19, s5, 0x16000
	s_mov_b32 m0, s19
	s_nop 0
	global_load_lds_dwordx4 v194, s[22:23]
	s_add_i32 s19, s5, 0x2000
	s_mov_b32 m0, s5
	s_nop 0
	global_load_lds_dwordx4 v1, s[8:9]
	s_add_u32 s24, s8, 0x40000
	s_mov_b32 m0, s19
	s_nop 0
	global_load_lds_dwordx4 v192, s[8:9]
	s_addc_u32 s25, s9, 0
	s_add_i32 s19, s5, 0x4000
	s_mov_b32 m0, s19
	s_nop 0
	global_load_lds_dwordx4 v1, s[24:25]
	s_add_i32 s19, s5, 0x6000
	s_mov_b32 m0, s19
	s_nop 0
	global_load_lds_dwordx4 v192, s[24:25]
	s_cmp_eq_u32 s15, 1
	s_mov_b32 s21, 0
	s_cselect_b64 s[22:23], -1, 0
	s_cmp_lg_u32 s15, 1
	s_cbranch_scc1 .LBB0_543
	s_barrier

; #define PG8_STAGE(bufoff, gbase, voff) do { PG8_GLDS((const char*)(gbase), (voff)[0], ldsb + (bufoff)); PG8_GLDS((const char*)(gbase), (voff)[1], ldsb + (bufoff) + 8192u); } while (0)
; #define PG8_STAGEA(bufoff, gbase, o0, o1) do { PG8_GLDS((const char*)(gbase), (o0), ldsb + (bufoff)); PG8_GLDS((const char*)(gbase), (o1), ldsb + (bufoff) + 8192u); } while (0)
; #define PG8_STAGEA1(bufoff, gbase) do { if constexpr (Sched::GATHER) { PG8_STAGEA(bufoff, gbase, vA2, vA3); } else { PG8_STAGEA(bufoff, (gbase) + hstep, vA0, vA1); } } while (0)
; template <class Epi, class Sched, bool F8 = false, bool PF = false, bool I8 = false, int PID = -1>
; __device__ __forceinline__ void gemm_phase(LAS unsigned char* lds, LAS unsigned char* xlds, const int RP, const int RPB, const int nt, const Sched& S, const Epi& E, const int stagger_ticks) {
;     ...
;         for (int t = 0; t < nt; t += 2) {
;             const bool last = (t == nt - 2);
;             unsigned ldsb = ldsb0; asm volatile("" : "+s"(ldsb));
;             const char* a1 = cA + (size_t)(t + 1) * kstep;
;             const char* a2 = last ? nA : cA + (size_t)(t + 2) * kstep; const char* b2 = last ? nB : cB + (size_t)(t + 2) * kstep;
;             const char* a3 = a2 + kstep; const char* b3 = b2 + kstep;
;             if constexpr (PF) { const char* pfa = (t + 4 < nt) ? cA + (size_t)(t + 4) * kstep : nA + (size_t)(t + 4 - nt) * kstep;
;                 asm volatile("s_mov_b32 m0, %2\n\ts_nop 0\n\tglobal_load_lds_dword %0, %1" :: "v"(voffP), "s"(pfa), "s"(ldsP) : "memory", "m0"); }
;             const bool relax = (Epi::RELAX > 0) && (t == 0) && epi_ran;
;             PG8_LDB(B0, 0, 0); PG8_LDB(B1, 0, 1); PG8_SCHED; PG8_LDA(At, 0, 0); PG8_STAGEA1(PG8_SA(1, 1), a1);
;             if (Sched::GATHER) { if (last) { const u32x4 nv = *nslot; vA0 = nv.x; vA1 = nv.y; vA2 = nv.z; vA3 = nv.w; } }
;             PG8_WAIT_VX(); PG8_WAIT_L(0); PG8_BAR; PG8_MMA(0, 0, At, B0); PG8_MMA(0, 1, At, B1); PG8_BAR; PG8_SCHED;
;             if constexpr (Epi::BIAS_DMA) { if (t == 0 && has_next) E.bias_dma(nxt, xlds + 8192 + ((ui + 1) & 1) * Epi::BIAS_STRIDE, wid, lane); }
;             PG8_LDA(At, 0, 1); PG8_STAGE(PG8_SB(0, 0), b2, voffB); PG8_STAGE(PG8_SB(0, 1), b2 + hstepB, voffB); PG8_STAGEA(PG8_SA(0, 0), a2, vA0, vA1);
;             PG8_WAIT_VX(); PG8_WAIT_L(0); PG8_BAR; PG8_MMA(1, 0, At, B0); PG8_MMA(1, 1, At, B1); PG8_BAR; PG8_SCHED;
.LBB0_546:
	s_mov_b64 s[36:37], s[10:11]
	s_add_u32 s20, s36, 0x100
	s_mov_b64 s[34:35], s[8:9]
	s_addc_u32 s45, s37, 0
	s_mov_b64 s[8:9], s[0:1]
	s_add_u32 s0, s34, 0x40080
	s_mov_b64 s[10:11], s[2:3]
	s_mov_b32 s15, s4
	s_mov_b32 s19, s6
	s_mov_b32 s6, s18
	s_mov_b32 s4, s14
	s_addc_u32 s1, s35, 0
	s_mov_b32 s46, -2
	s_mov_b32 s47, s5
	v_add_u32_e32 v142, 0x10000, v195
	v_add_u32_e32 v158, 0x14000, v195
	ds_read_b128 v[130:133], v142
	ds_read_b128 v[134:137], v142 offset:1024
	ds_read_b128 v[138:141], v142 offset:2048
	ds_read_b128 v[142:145], v142 offset:3072
	ds_read_b128 v[146:149], v158
	ds_read_b128 v[150:153], v158 offset:1024
	ds_read_b128 v[154:157], v158 offset:2048
	ds_read_b128 v[158:161], v158 offset:3072
	s_add_u32 s2, s0, 0xfffc0080
	s_addc_u32 s3, s1, -1
	s_cmp_eq_u32 s46, 12
	s_cselect_b32 s36, s8, s2
	s_cselect_b32 s37, s9, s3
	s_cselect_b32 s34, s10, s20
	s_cselect_b32 s35, s11, s45
	s_add_u32 s2, s36, 0x80
	s_addc_u32 s3, s37, 0
	ds_read_b128 v[162:165], v196
	ds_read_b128 v[166:169], v196 offset:1024
	ds_read_b128 v[170:173], v196 offset:2048
	ds_read_b128 v[174:177], v196 offset:3072
	ds_read_b128 v[180:183], v196 offset:4096
	ds_read_b128 v[184:187], v196 offset:5120
	ds_read_b128 v[188:191], v196 offset:6144
	ds_read_b128 v[198:201], v196 offset:7168
	s_add_i32 s48, s47, 0xc000
	s_mov_b32 m0, s48
	s_nop 0
	global_load_lds_dwordx4 v1, s[0:1]
	s_add_i32 s48, s47, 0xe000
	s_mov_b32 m0, s48
	s_nop 0
	global_load_lds_dwordx4 v192, s[0:1]
	s_waitcnt vmcnt(8)
	s_waitcnt lgkmcnt(0)
	s_barrier
	s_setprio 1
	s_waitcnt lgkmcnt(7)
	v_mfma_f32_16x16x32_bf16 v[114:117], v[130:133], v[162:165], 0
	v_mfma_f32_16x16x32_bf16 v[118:121], v[138:141], v[162:165], 0
	s_waitcnt lgkmcnt(5)
	v_mfma_f32_16x16x32_bf16 v[110:113], v[130:133], v[170:173], 0
	v_mfma_f32_16x16x32_bf16 v[106:109], v[138:141], v[170:173], 0
	s_waitcnt lgkmcnt(3)
	v_mfma_f32_16x16x32_bf16 v[94:97], v[130:133], v[180:183], 0
	v_mfma_f32_16x16x32_bf16 v[90:93], v[138:141], v[180:183], 0
	s_waitcnt lgkmcnt(1)
	v_mfma_f32_16x16x32_bf16 v[78:81], v[130:133], v[188:191], 0
	v_mfma_f32_16x16x32_bf16 v[74:77], v[138:141], v[188:191], 0
	v_mfma_f32_16x16x32_bf16 v[114:117], v[134:137], v[166:169], v[114:117]
	v_mfma_f32_16x16x32_bf16 v[118:121], v[142:145], v[166:169], v[118:121]
	v_mfma_f32_16x16x32_bf16 v[110:113], v[134:137], v[174:177], v[110:113]
	v_mfma_f32_16x16x32_bf16 v[106:109], v[142:145], v[174:177], v[106:109]
	v_mfma_f32_16x16x32_bf16 v[94:97], v[134:137], v[184:187], v[94:97]
	v_mfma_f32_16x16x32_bf16 v[90:93], v[142:145], v[184:187], v[90:93]
	s_waitcnt lgkmcnt(0)
	v_mfma_f32_16x16x32_bf16 v[78:81], v[134:137], v[198:201], v[78:81]
	v_mfma_f32_16x16x32_bf16 v[74:77], v[142:145], v[198:201], v[74:77]
	s_setprio 0
	s_setprio 1
	v_mfma_f32_16x16x32_bf16 v[126:129], v[146:149], v[162:165], 0
	v_mfma_f32_16x16x32_bf16 v[122:125], v[154:157], v[162:165], 0
	v_mfma_f32_16x16x32_bf16 v[102:105], v[146:149], v[170:173], 0
	v_mfma_f32_16x16x32_bf16 v[98:101], v[154:157], v[170:173], 0
	v_mfma_f32_16x16x32_bf16 v[86:89], v[146:149], v[180:183], 0
	v_mfma_f32_16x16x32_bf16 v[82:85], v[154:157], v[180:183], 0
	v_mfma_f32_16x16x32_bf16 v[70:73], v[146:149], v[188:191], 0
	v_mfma_f32_16x16x32_bf16 v[66:69], v[154:157], v[188:191], 0
	v_mfma_f32_16x16x32_bf16 v[126:129], v[150:153], v[166:169], v[126:129]
	v_mfma_f32_16x16x32_bf16 v[122:125], v[158:161], v[166:169], v[122:125]
	v_mfma_f32_16x16x32_bf16 v[102:105], v[150:153], v[174:177], v[102:105]
	v_mfma_f32_16x16x32_bf16 v[98:101], v[158:161], v[174:177], v[98:101]
	v_mfma_f32_16x16x32_bf16 v[86:89], v[150:153], v[184:187], v[86:89]
	v_mfma_f32_16x16x32_bf16 v[82:85], v[158:161], v[184:187], v[82:85]
	v_mfma_f32_16x16x32_bf16 v[70:73], v[150:153], v[198:201], v[70:73]
	v_mfma_f32_16x16x32_bf16 v[66:69], v[158:161], v[198:201], v[66:69]
	s_setprio 0
	s_barrier
	ds_read_b128 v[162:165], v196 offset:16384
	ds_read_b128 v[166:169], v196 offset:17408
	ds_read_b128 v[170:173], v196 offset:18432
	ds_read_b128 v[174:177], v196 offset:19456
	ds_read_b128 v[180:183], v196 offset:20480
	ds_read_b128 v[184:187], v196 offset:21504
	ds_read_b128 v[188:191], v196 offset:22528
	ds_read_b128 v[198:201], v196 offset:23552
	s_add_i32 s48, s47, 0x10000
	s_mov_b32 m0, s48
	s_nop 0
	global_load_lds_dwordx4 v193, s[34:35]
	s_add_i32 s48, s47, 0x12000
	s_mov_b32 m0, s48
	s_nop 0
	global_load_lds_dwordx4 v194, s[34:35]
	s_add_u32 s48, s34, 0x4000
	s_addc_u32 s49, s35, 0
	s_add_i32 s50, s47, 0x14000
	s_mov_b32 m0, s50
	s_nop 0
	global_load_lds_dwordx4 v193, s[48:49]
	s_add_i32 s50, s47, 0x16000
	s_mov_b32 m0, s50
	s_nop 0
	global_load_lds_dwordx4 v194, s[48:49]
	s_add_i32 s48, s47, 0x2000
	s_mov_b32 m0, s47
	s_nop 0
	global_load_lds_dwordx4 v1, s[36:37]
	s_nop 0
	s_mov_b32 m0, s48
	s_nop 0
	global_load_lds_dwordx4 v192, s[36:37]
	s_waitcnt vmcnt(8)
	s_waitcnt lgkmcnt(0)
	s_barrier
; #define PG8_STAGE(bufoff, gbase, voff) do { PG8_GLDS((const char*)(gbase), (voff)[0], ldsb + (bufoff)); PG8_GLDS((const char*)(gbase), (voff)[1], ldsb + (bufoff) + 8192u); } while (0)
; #define PG8_STAGEA(bufoff, gbase, o0, o1) do { PG8_GLDS((const char*)(gbase), (o0), ldsb + (bufoff)); PG8_GLDS((const char*)(gbase), (o1), ldsb + (bufoff) + 8192u); } while (0)
; #define PG8_STAGEA1(bufoff, gbase) do { if constexpr (Sched::GATHER) { PG8_STAGEA(bufoff, gbase, vA2, vA3); } else { PG8_STAGEA(bufoff, (gbase) + hstep, vA0, vA1); } } while (0)
; #define PG8_LDA(dst, b, h) do { if constexpr (F8) { _Pragma("unroll") for (int m = 0; m < 4; ++m) dst##8[m] = PG8_LD32(lds + PG8_SA(b, h) + aoff + m * 2048); } else { \
;         _Pragma("unroll") for (int m = 0; m < 4; ++m) _Pragma("unroll") for (int k = 0; k < 2; ++k) dst[m][k] = *(const LAS bf16x8*)(lds + PG8_SA(b, h) + aoff + m * 2048 + k * 1024); } } while (0)
; #define PG8_WAIT_VR() PG8_WAIT_V(8)
; #define PG8_WAIT_L(n) asm volatile("s_waitcnt lgkmcnt(" #n ")" ::: "memory")
; template <class Epi, class Sched, bool F8 = false, bool PF = false, bool I8 = false, int PID = -1>
; __device__ __forceinline__ void gemm_phase(LAS unsigned char* lds, LAS unsigned char* xlds, const int RP, const int RPB, const int nt, const Sched& S, const Epi& E, const int stagger_ticks) {
;     ...
;             PG8_WAIT_VX(); PG8_WAIT_L(0); PG8_BAR; PG8_MMA(0, 0, At, B0); PG8_MMA(0, 1, At, B1); PG8_BAR; PG8_SCHED;
;             if constexpr (Epi::BIAS_DMA) { if (t == 0 && has_next) E.bias_dma(nxt, xlds + 8192 + ((ui + 1) & 1) * Epi::BIAS_STRIDE, wid, lane); }
;             PG8_LDA(At, 0, 1); PG8_STAGE(PG8_SB(0, 0), b2, voffB); PG8_STAGE(PG8_SB(0, 1), b2 + hstepB, voffB); PG8_STAGEA(PG8_SA(0, 0), a2, vA0, vA1);
;             PG8_WAIT_VX(); PG8_WAIT_L(0); PG8_BAR; PG8_MMA(1, 0, At, B0); PG8_MMA(1, 1, At, B1); PG8_BAR; PG8_SCHED;
;             PG8_LDB(B0, 1, 0); PG8_LDB(B1, 1, 1); PG8_SCHED; PG8_LDA(At, 1, 0); PG8_STAGEA1(PG8_SA(0, 1), a2);
;             PG8_WAIT_VR(); PG8_WAIT_L(0); PG8_BAR; PG8_MMA(0, 0, At, B0); PG8_MMA(0, 1, At, B1); PG8_BAR; PG8_SCHED;
;             PG8_LDA(At, 1, 1); PG8_STAGE(PG8_SB(1, 0), b3, voffB); PG8_STAGE(PG8_SB(1, 1), b3 + hstepB, voffB); PG8_STAGEA(PG8_SA(1, 0), a3, vA0, vA1);
;             PG8_WAIT_VR(); PG8_WAIT_L(0); PG8_BAR; PG8_MMA(1, 0, At, B0); PG8_MMA(1, 1, At, B1); PG8_BAR; PG8_SCHED;
	s_setprio 1
	s_waitcnt lgkmcnt(7)
	v_mfma_f32_16x16x32_bf16 v[50:53], v[130:133], v[162:165], 0
	v_mfma_f32_16x16x32_bf16 v[54:57], v[138:141], v[162:165], 0
	s_waitcnt lgkmcnt(5)
	v_mfma_f32_16x16x32_bf16 v[46:49], v[130:133], v[170:173], 0
	v_mfma_f32_16x16x32_bf16 v[42:45], v[138:141], v[170:173], 0
	s_waitcnt lgkmcnt(3)
	v_mfma_f32_16x16x32_bf16 v[30:33], v[130:133], v[180:183], 0
	v_mfma_f32_16x16x32_bf16 v[26:29], v[138:141], v[180:183], 0
	s_waitcnt lgkmcnt(1)
	v_mfma_f32_16x16x32_bf16 v[14:17], v[130:133], v[188:191], 0
	v_mfma_f32_16x16x32_bf16 v[10:13], v[138:141], v[188:191], 0
	v_mfma_f32_16x16x32_bf16 v[50:53], v[134:137], v[166:169], v[50:53]
	v_mfma_f32_16x16x32_bf16 v[54:57], v[142:145], v[166:169], v[54:57]
	v_mfma_f32_16x16x32_bf16 v[46:49], v[134:137], v[174:177], v[46:49]
	v_mfma_f32_16x16x32_bf16 v[42:45], v[142:145], v[174:177], v[42:45]
	v_mfma_f32_16x16x32_bf16 v[30:33], v[134:137], v[184:187], v[30:33]
	v_mfma_f32_16x16x32_bf16 v[26:29], v[142:145], v[184:187], v[26:29]
	s_waitcnt lgkmcnt(0)
	v_mfma_f32_16x16x32_bf16 v[14:17], v[134:137], v[198:201], v[14:17]
	v_mfma_f32_16x16x32_bf16 v[10:13], v[142:145], v[198:201], v[10:13]
	s_setprio 0
	s_setprio 1
	v_mfma_f32_16x16x32_bf16 v[58:61], v[146:149], v[162:165], 0
	v_mfma_f32_16x16x32_bf16 v[62:65], v[154:157], v[162:165], 0
	v_mfma_f32_16x16x32_bf16 v[38:41], v[146:149], v[170:173], 0
	v_mfma_f32_16x16x32_bf16 v[34:37], v[154:157], v[170:173], 0
	v_mfma_f32_16x16x32_bf16 v[22:25], v[146:149], v[180:183], 0
	v_mfma_f32_16x16x32_bf16 v[18:21], v[154:157], v[180:183], 0
	v_mfma_f32_16x16x32_bf16 v[6:9], v[146:149], v[188:191], 0
	v_mfma_f32_16x16x32_bf16 v[2:5], v[154:157], v[188:191], 0
	v_mfma_f32_16x16x32_bf16 v[58:61], v[150:153], v[166:169], v[58:61]
	v_mfma_f32_16x16x32_bf16 v[62:65], v[158:161], v[166:169], v[62:65]
	v_mfma_f32_16x16x32_bf16 v[38:41], v[150:153], v[174:177], v[38:41]
	v_mfma_f32_16x16x32_bf16 v[34:37], v[158:161], v[174:177], v[34:37]
	v_mfma_f32_16x16x32_bf16 v[22:25], v[150:153], v[184:187], v[22:25]
	v_mfma_f32_16x16x32_bf16 v[18:21], v[158:161], v[184:187], v[18:21]
	v_mfma_f32_16x16x32_bf16 v[6:9], v[150:153], v[198:201], v[6:9]
	v_mfma_f32_16x16x32_bf16 v[2:5], v[158:161], v[198:201], v[2:5]
	s_setprio 0
	s_barrier
	v_add_u32_e32 v142, 0x18000, v195
	v_add_u32_e32 v158, 0x1c000, v195
	ds_read_b128 v[130:133], v142
	ds_read_b128 v[134:137], v142 offset:1024
	ds_read_b128 v[138:141], v142 offset:2048
	ds_read_b128 v[142:145], v142 offset:3072
	ds_read_b128 v[146:149], v158
	ds_read_b128 v[150:153], v158 offset:1024
	ds_read_b128 v[154:157], v158 offset:2048
	ds_read_b128 v[158:161], v158 offset:3072
	ds_read_b128 v[162:165], v196 offset:32768
	ds_read_b128 v[166:169], v196 offset:33792
	ds_read_b128 v[170:173], v196 offset:34816
	ds_read_b128 v[174:177], v196 offset:35840
	ds_read_b128 v[180:183], v196 offset:36864
	ds_read_b128 v[184:187], v196 offset:37888
	ds_read_b128 v[188:191], v196 offset:38912
	ds_read_b128 v[198:201], v196 offset:39936
	s_add_u32 s36, s36, 0x40000
	s_addc_u32 s37, s37, 0
	s_add_i32 s48, s47, 0x4000
	s_mov_b32 m0, s48
	s_nop 0
	global_load_lds_dwordx4 v1, s[36:37]
	s_add_i32 s48, s47, 0x6000
	s_mov_b32 m0, s48
	s_nop 0
	global_load_lds_dwordx4 v192, s[36:37]
	s_waitcnt vmcnt(8)
	s_waitcnt lgkmcnt(0)
	s_barrier
	s_setprio 1
	s_waitcnt lgkmcnt(7)
	v_mfma_f32_16x16x32_bf16 v[114:117], v[130:133], v[162:165], v[114:117]
	v_mfma_f32_16x16x32_bf16 v[118:121], v[138:141], v[162:165], v[118:121]
	s_waitcnt lgkmcnt(5)
	v_mfma_f32_16x16x32_bf16 v[110:113], v[130:133], v[170:173], v[110:113]
	v_mfma_f32_16x16x32_bf16 v[106:109], v[138:141], v[170:173], v[106:109]
	s_waitcnt lgkmcnt(3)
	v_mfma_f32_16x16x32_bf16 v[94:97], v[130:133], v[180:183], v[94:97]
	v_mfma_f32_16x16x32_bf16 v[90:93], v[138:141], v[180:183], v[90:93]
	s_waitcnt lgkmcnt(1)
	v_mfma_f32_16x16x32_bf16 v[78:81], v[130:133], v[188:191], v[78:81]
	v_mfma_f32_16x16x32_bf16 v[74:77], v[138:141], v[188:191], v[74:77]
	v_mfma_f32_16x16x32_bf16 v[114:117], v[134:137], v[166:169], v[114:117]
	v_mfma_f32_16x16x32_bf16 v[118:121], v[142:145], v[166:169], v[118:121]
	v_mfma_f32_16x16x32_bf16 v[110:113], v[134:137], v[174:177], v[110:113]
	v_mfma_f32_16x16x32_bf16 v[106:109], v[142:145], v[174:177], v[106:109]
	v_mfma_f32_16x16x32_bf16 v[94:97], v[134:137], v[184:187], v[94:97]
	v_mfma_f32_16x16x32_bf16 v[90:93], v[142:145], v[184:187], v[90:93]
	s_waitcnt lgkmcnt(0)
	v_mfma_f32_16x16x32_bf16 v[78:81], v[134:137], v[198:201], v[78:81]
	v_mfma_f32_16x16x32_bf16 v[74:77], v[142:145], v[198:201], v[74:77]
	s_setprio 0
	s_setprio 1
	v_mfma_f32_16x16x32_bf16 v[126:129], v[146:149], v[162:165], v[126:129]
	v_mfma_f32_16x16x32_bf16 v[122:125], v[154:157], v[162:165], v[122:125]
	v_mfma_f32_16x16x32_bf16 v[102:105], v[146:149], v[170:173], v[102:105]
	v_mfma_f32_16x16x32_bf16 v[98:101], v[154:157], v[170:173], v[98:101]
	v_mfma_f32_16x16x32_bf16 v[86:89], v[146:149], v[180:183], v[86:89]
	v_mfma_f32_16x16x32_bf16 v[82:85], v[154:157], v[180:183], v[82:85]
	v_mfma_f32_16x16x32_bf16 v[70:73], v[146:149], v[188:191], v[70:73]
	v_mfma_f32_16x16x32_bf16 v[66:69], v[154:157], v[188:191], v[66:69]
	v_mfma_f32_16x16x32_bf16 v[126:129], v[150:153], v[166:169], v[126:129]
	v_mfma_f32_16x16x32_bf16 v[122:125], v[158:161], v[166:169], v[122:125]
	v_mfma_f32_16x16x32_bf16 v[102:105], v[150:153], v[174:177], v[102:105]
	v_mfma_f32_16x16x32_bf16 v[98:101], v[158:161], v[174:177], v[98:101]
	v_mfma_f32_16x16x32_bf16 v[86:89], v[150:153], v[184:187], v[86:89]
	v_mfma_f32_16x16x32_bf16 v[82:85], v[158:161], v[184:187], v[82:85]
	v_mfma_f32_16x16x32_bf16 v[70:73], v[150:153], v[198:201], v[70:73]
	v_mfma_f32_16x16x32_bf16 v[66:69], v[158:161], v[198:201], v[66:69]
	s_setprio 0
	s_barrier
; #define PG8_STAGE(bufoff, gbase, voff) do { PG8_GLDS((const char*)(gbase), (voff)[0], ldsb + (bufoff)); PG8_GLDS((const char*)(gbase), (voff)[1], ldsb + (bufoff) + 8192u); } while (0)
; #define PG8_STAGEA(bufoff, gbase, o0, o1) do { PG8_GLDS((const char*)(gbase), (o0), ldsb + (bufoff)); PG8_GLDS((const char*)(gbase), (o1), ldsb + (bufoff) + 8192u); } while (0)
; #define PG8_LDA(dst, b, h) do { if constexpr (F8) { _Pragma("unroll") for (int m = 0; m < 4; ++m) dst##8[m] = PG8_LD32(lds + PG8_SA(b, h) + aoff + m * 2048); } else { \
;         _Pragma("unroll") for (int m = 0; m < 4; ++m) _Pragma("unroll") for (int k = 0; k < 2; ++k) dst[m][k] = *(const LAS bf16x8*)(lds + PG8_SA(b, h) + aoff + m * 2048 + k * 1024); } } while (0)
; #define PG8_WAIT_VR() PG8_WAIT_V(8)
; #define PG8_WAIT_L(n) asm volatile("s_waitcnt lgkmcnt(" #n ")" ::: "memory")
; #define PG8_BAR __builtin_amdgcn_s_barrier()
; #define PG8_SCHED __builtin_amdgcn_sched_barrier(0)
; template <class Epi, class Sched, bool F8 = false, bool PF = false, bool I8 = false, int PID = -1>
; __device__ __forceinline__ void gemm_phase(LAS unsigned char* lds, LAS unsigned char* xlds, const int RP, const int RPB, const int nt, const Sched& S, const Epi& E, const int stagger_ticks) {
;     ...
;             PG8_LDA(At, 1, 1); PG8_STAGE(PG8_SB(1, 0), b3, voffB); PG8_STAGE(PG8_SB(1, 1), b3 + hstepB, voffB); PG8_STAGEA(PG8_SA(1, 0), a3, vA0, vA1);
;             PG8_WAIT_VR(); PG8_WAIT_L(0); PG8_BAR; PG8_MMA(1, 0, At, B0); PG8_MMA(1, 1, At, B1); PG8_BAR; PG8_SCHED;
;         }
	s_add_u32 s36, s34, 0x80
	ds_read_b128 v[162:165], v196 offset:49152
	ds_read_b128 v[166:169], v196 offset:50176
	ds_read_b128 v[170:173], v196 offset:51200
	ds_read_b128 v[174:177], v196 offset:52224
	ds_read_b128 v[180:183], v196 offset:53248
	ds_read_b128 v[184:187], v196 offset:54272
	ds_read_b128 v[188:191], v196 offset:55296
	ds_read_b128 v[198:201], v196 offset:56320
	s_addc_u32 s37, s35, 0
	s_add_i32 s48, s47, 0x18000
	s_mov_b32 m0, s48
	s_nop 0
	global_load_lds_dwordx4 v193, s[36:37]
	s_add_i32 s48, s47, 0x1a000
	s_mov_b32 m0, s48
	s_nop 0
	global_load_lds_dwordx4 v194, s[36:37]
	s_add_u32 s34, s34, 0x4080
	s_addc_u32 s35, s35, 0
	s_add_i32 s36, s47, 0x1c000
	s_mov_b32 m0, s36
	s_nop 0
	global_load_lds_dwordx4 v193, s[34:35]
	s_add_i32 s36, s47, 0x1e000
	s_mov_b32 m0, s36
	s_nop 0
	global_load_lds_dwordx4 v194, s[34:35]
	s_add_i32 s34, s47, 0x8000
	s_mov_b32 m0, s34
	s_nop 0
	global_load_lds_dwordx4 v1, s[2:3]
	s_add_i32 s47, s47, 0xa000
	s_mov_b32 m0, s47
	s_nop 0
	global_load_lds_dwordx4 v192, s[2:3]
	s_waitcnt vmcnt(8)
	s_waitcnt lgkmcnt(0)
	s_barrier
	s_setprio 1
	s_waitcnt lgkmcnt(7)
	v_mfma_f32_16x16x32_bf16 v[50:53], v[130:133], v[162:165], v[50:53]
	v_mfma_f32_16x16x32_bf16 v[54:57], v[138:141], v[162:165], v[54:57]
	s_waitcnt lgkmcnt(5)
	v_mfma_f32_16x16x32_bf16 v[46:49], v[130:133], v[170:173], v[46:49]
	v_mfma_f32_16x16x32_bf16 v[42:45], v[138:141], v[170:173], v[42:45]
	s_waitcnt lgkmcnt(3)
	v_mfma_f32_16x16x32_bf16 v[30:33], v[130:133], v[180:183], v[30:33]
	v_mfma_f32_16x16x32_bf16 v[26:29], v[138:141], v[180:183], v[26:29]
	s_waitcnt lgkmcnt(1)
	v_mfma_f32_16x16x32_bf16 v[14:17], v[130:133], v[188:191], v[14:17]
	v_mfma_f32_16x16x32_bf16 v[10:13], v[138:141], v[188:191], v[10:13]
	v_mfma_f32_16x16x32_bf16 v[50:53], v[134:137], v[166:169], v[50:53]
	v_mfma_f32_16x16x32_bf16 v[54:57], v[142:145], v[166:169], v[54:57]
	v_mfma_f32_16x16x32_bf16 v[46:49], v[134:137], v[174:177], v[46:49]
	v_mfma_f32_16x16x32_bf16 v[42:45], v[142:145], v[174:177], v[42:45]
	v_mfma_f32_16x16x32_bf16 v[30:33], v[134:137], v[184:187], v[30:33]
	v_mfma_f32_16x16x32_bf16 v[26:29], v[142:145], v[184:187], v[26:29]
	s_waitcnt lgkmcnt(0)
	v_mfma_f32_16x16x32_bf16 v[14:17], v[134:137], v[198:201], v[14:17]
	v_mfma_f32_16x16x32_bf16 v[10:13], v[142:145], v[198:201], v[10:13]
	s_setprio 0
	s_setprio 1
	v_mfma_f32_16x16x32_bf16 v[58:61], v[146:149], v[162:165], v[58:61]
	v_mfma_f32_16x16x32_bf16 v[62:65], v[154:157], v[162:165], v[62:65]
	v_mfma_f32_16x16x32_bf16 v[38:41], v[146:149], v[170:173], v[38:41]
	v_mfma_f32_16x16x32_bf16 v[34:37], v[154:157], v[170:173], v[34:37]
	v_mfma_f32_16x16x32_bf16 v[22:25], v[146:149], v[180:183], v[22:25]
	v_mfma_f32_16x16x32_bf16 v[18:21], v[154:157], v[180:183], v[18:21]
	v_mfma_f32_16x16x32_bf16 v[6:9], v[146:149], v[188:191], v[6:9]
	v_mfma_f32_16x16x32_bf16 v[2:5], v[154:157], v[188:191], v[2:5]
	v_mfma_f32_16x16x32_bf16 v[58:61], v[150:153], v[166:169], v[58:61]
	v_mfma_f32_16x16x32_bf16 v[62:65], v[158:161], v[166:169], v[62:65]
	v_mfma_f32_16x16x32_bf16 v[38:41], v[150:153], v[174:177], v[38:41]
	v_mfma_f32_16x16x32_bf16 v[34:37], v[158:161], v[174:177], v[34:37]
	v_mfma_f32_16x16x32_bf16 v[22:25], v[150:153], v[184:187], v[22:25]
	v_mfma_f32_16x16x32_bf16 v[18:21], v[158:161], v[184:187], v[18:21]
	v_mfma_f32_16x16x32_bf16 v[6:9], v[150:153], v[198:201], v[6:9]
	v_mfma_f32_16x16x32_bf16 v[2:5], v[158:161], v[198:201], v[2:5]
	s_setprio 0
	s_barrier
	s_add_i32 s46, s46, 2
	s_add_u32 s20, s20, 0x100
	s_addc_u32 s45, s45, 0
	s_add_u32 s0, s0, 0x100
	s_addc_u32 s1, s1, 0
	s_cmp_gt_u32 s46, 13

; #define PG8_UNI64(p) ((const char*)((((unsigned long long)(unsigned)__builtin_amdgcn_readfirstlane((int)((unsigned long long)(p) >> 32))) << 32) | (unsigned long long)(unsigned)__builtin_amdgcn_readfirstlane((int)(unsigned)(unsigned long long)(p))))
; #define PG8_BAR __builtin_amdgcn_s_barrier()
;     __device__ __forceinline__ const char* Abase(const pg8::Unit& u) const { size_t o = WS_R1; if (u.aux == 1) o = WS_R3; return ws + o + (size_t)u.pm * TSF8; }
;     __device__ __forceinline__ const char* Bbase(const pg8::Unit& u) const { size_t o = WS_WIN; if (u.aux == 1) o = WS_WKV; return ws + o + (size_t)u.pn * TSF8; }
;     __device__ __forceinline__ const char* Abase(const pg8::Unit& u) const { if (GATH) return ws + WS_XQ; return ws + WS_H2 + (size_t)u.pm * TSF8; }
; template <class Epi, class Sched, bool F8 = false, bool PF = false, bool I8 = false, int PID = -1>
; __device__ __forceinline__ void gemm_phase(LAS unsigned char* lds, LAS unsigned char* xlds, const int RP, const int RPB, const int nt, const Sched& S, const Epi& E, const int stagger_ticks) {
;     ...
;         cur = nxt; cA = nA; cB = nB; ++ui;
;         has_next = has_nn; nxt = nn;
;         if (has_next) { nA = PG8_UNI64(S.Abase(nxt)); nB = PG8_UNI64(S.Bbase(nxt)); }
;         if (Sched::GATHER) { *nslot = (u32x4){gv[0], gv[1], gv[2], gv[3]}; asm volatile("" ::: "memory"); }
;         PG8_ZERO_ACC();
;         if (wr == 1) PG8_BAR;
.LBB0_573:
	v_mov_b32_e32 v179, v178
	v_mov_b64_e32 v[130:131], v[178:179]
	s_andn2_b64 vcc, exec, s[22:23]
	s_waitcnt lgkmcnt(0)
	s_cbranch_vccnz .LBB0_544
	s_barrier
	s_branch .LBB0_544

; #define PG8_STAGE(bufoff, gbase, voff) do { PG8_GLDS((const char*)(gbase), (voff)[0], ldsb + (bufoff)); PG8_GLDS((const char*)(gbase), (voff)[1], ldsb + (bufoff) + 8192u); } while (0)
; #define PG8_STAGEA(bufoff, gbase, o0, o1) do { PG8_GLDS((const char*)(gbase), (o0), ldsb + (bufoff)); PG8_GLDS((const char*)(gbase), (o1), ldsb + (bufoff) + 8192u); } while (0)
; #define PG8_STAGEA1(bufoff, gbase) do { if constexpr (Sched::GATHER) { PG8_STAGEA(bufoff, gbase, vA2, vA3); } else { PG8_STAGEA(bufoff, (gbase) + hstep, vA0, vA1); } } while (0)
; #define PG8_BAR __builtin_amdgcn_s_barrier()
; template <class Epi, class Sched, bool F8 = false, bool PF = false, bool I8 = false, int PID = -1>
; __device__ __forceinline__ void gemm_phase(LAS unsigned char* lds, LAS unsigned char* xlds, const int RP, const int RPB, const int nt, const Sched& S, const Epi& E, const int stagger_ticks) {
;     ...
;     for (int i = 0; i < 2; ++i) { int R, C; stage_rc(tid * 16 + i * 8192, R, C); Rr[i] = R; Cc[i] = C; const int Rb = Epi::PERM ? permB(R) : R; voffB[i] = (unsigned)(Rb * RPB + C * 2); }
;     const size_t kstep = (size_t)(BK * 2);
;     const size_t hstep = (size_t)HALF * RP, hstepB = (size_t)(Epi::PERM ? 8 : HALF) * RPB;
;     const unsigned ldsw = (unsigned)wid * 1024u;
;     const unsigned ldsb0 = (unsigned)__builtin_amdgcn_readfirstlane((int)(unsigned)(size_t)lds) + ldsw; const unsigned ldsb = ldsb0;
;     const int aoff = lds_byte(wr * 64 + fr, fq * 8), boff = lds_byte(wc * 32 + fr, fq * 8);
;     const unsigned voffP = (unsigned)((32 * wid + (lane & 31)) * RP + (lane >> 5) * 128);
;     ...
;     PG8_ZERO_ACC();
;     PG8_STAGE(PG8_SB(0, 0), cB, voffB); PG8_STAGE(PG8_SB(0, 1), cB + hstepB, voffB); PG8_STAGEA(PG8_SA(0, 0), cA, vA0, vA1); PG8_STAGEA1(PG8_SA(0, 1), cA);
;     if (wr == 1) PG8_BAR;
.LBB0_635:
	v_bfe_i32 v3, v132, 27, 1
	v_lshlrev_b32_e32 v1, 4, v132
	v_lshrrev_b32_e32 v3, 22, v3
	v_add_u32_e32 v3, v1, v3
	v_and_b32_e32 v3, 0xfffffc00, v3
	v_sub_u32_e32 v3, v1, v3
	v_lshrrev_b32_e32 v4, 4, v3
	v_bitop3_b32 v3, v4, v3, 32 bitop3:0x6c
	v_ashrrev_i32_e32 v5, 31, v3
	v_ashrrev_i32_e32 v2, 31, v132
	v_lshrrev_b32_e32 v5, 26, v5
	v_lshrrev_b32_e32 v2, 26, v2
	v_add_u32_e32 v5, v3, v5
	v_add_u32_e32 v2, v132, v2
	s_waitcnt vmcnt(6)
	v_ashrrev_i32_e32 v6, 6, v5
	v_and_b32_e32 v5, 0xc0, v5
	v_ashrrev_i32_e32 v2, 6, v2
	v_sub_u32_e32 v3, v3, v5
	v_mov_b32_e32 v5, 1
	v_lshlrev_b32_e32 v4, 3, v2
	v_lshlrev_b32_e32 v2, 5, v2
	v_ashrrev_i16_sdwa v3, v5, sext(v3) dst_sel:DWORD dst_unused:UNUSED_PAD src0_sel:DWORD src1_sel:BYTE_0
	v_and_b32_e32 v2, 32, v2
	v_bfe_i32 v3, v3, 0, 16
	v_add_u32_e32 v1, 0x2000, v1
	v_add_lshl_u32 v2, v2, v3, 1
	v_ashrrev_i32_e32 v3, 31, v1
	v_lshrrev_b32_e32 v3, 22, v3
	v_add_u32_e32 v3, v1, v3
	v_ashrrev_i32_e32 v3, 10, v3
	v_mul_i32_i24_e32 v7, 0x400, v3
	v_sub_u32_e32 v1, v1, v7
	v_lshrrev_b32_e32 v7, 4, v1
	v_bitop3_b32 v1, v7, v1, 32 bitop3:0x6c
	v_ashrrev_i32_e32 v8, 31, v1
	v_lshrrev_b32_e32 v8, 26, v8
	v_add_u32_e32 v8, v1, v8
	v_ashrrev_i32_e32 v9, 6, v8
	v_and_b32_e32 v8, 0xc0, v8
	v_sub_u32_e32 v1, v1, v8
	v_and_b32_e32 v4, -16, v4
	v_lshlrev_b32_e32 v7, 3, v3
	v_lshlrev_b32_e32 v3, 5, v3
	v_ashrrev_i16_sdwa v1, v5, sext(v1) dst_sel:DWORD dst_unused:UNUSED_PAD src0_sel:DWORD src1_sel:BYTE_0
	v_add_u32_e32 v4, v6, v4
	v_and_b32_e32 v3, 32, v3
	v_bfe_i32 v1, v1, 0, 16
	v_add_lshl_u32 v3, v3, v1, 1
	v_lshl_add_u32 v1, v4, 10, v2
	v_lshlrev_b32_e32 v5, 1, v4
	v_lshlrev_b32_e32 v8, 2, v4
	v_lshrrev_b32_e32 v4, 2, v4
	v_and_b32_e32 v6, 3, v6
	v_and_b32_e32 v7, -16, v7
	v_and_b32_e32 v5, 0x3fffc0, v5
	v_and_b32_e32 v4, 4, v4
	v_and_or_b32 v6, v8, 48, v6
	v_add_u32_e32 v7, v9, v7
	v_or3_b32 v4, v6, v5, v4
	s_ashr_i32 s5, s4, 6
	v_lshl_add_u32 v195, v4, 10, v2
	v_lshlrev_b32_e32 v2, 1, v7
	v_lshlrev_b32_e32 v4, 2, v7
	v_lshrrev_b32_e32 v5, 2, v7
	v_and_b32_e32 v6, 3, v9
	v_mov_b32_e32 v130, 0
	v_and_b32_e32 v2, 0x3fffc0, v2
	v_and_b32_e32 v5, 4, v5
	v_and_or_b32 v4, v4, 48, v6
	s_lshl_b32 s16, s5, 10
	v_mov_b32_e32 v131, v130
	v_or3_b32 v2, v4, v2, v5
	s_add_i32 s29, s16, 0
	v_mov_b64_e32 v[134:135], v[130:131]
	v_lshl_add_u32 v194, v7, 10, v3
	v_lshl_add_u32 v196, v2, 10, v3
	s_add_i32 s16, s29, 0x10000
	s_waitcnt vmcnt(2)
	s_waitcnt vmcnt(0)
	s_ashr_i32 s15, s4, 8
	s_mov_b32 m0, s16
	s_nop 0
	global_load_lds_dwordx4 v195, s[10:11]
	s_add_i32 s16, s29, 0x12000
	s_mov_b32 m0, s16
	s_nop 0
	global_load_lds_dwordx4 v196, s[10:11]
	s_add_u32 s16, s10, 0x2000
	s_addc_u32 s17, s11, 0
	s_add_i32 s18, s29, 0x14000
	s_mov_b32 m0, s18
	s_nop 0
	global_load_lds_dwordx4 v195, s[16:17]
	s_add_i32 s18, s29, 0x16000
	s_mov_b32 m0, s18
	s_nop 0
	global_load_lds_dwordx4 v196, s[16:17]
	s_add_i32 s16, s29, 0x2000
	s_mov_b32 m0, s29
	s_nop 0
	global_load_lds_dwordx4 v1, s[8:9]
	s_add_u32 s18, s8, 0x20000
	s_mov_b32 m0, s16
	s_nop 0
	global_load_lds_dwordx4 v194, s[8:9]
	s_addc_u32 s19, s9, 0
	s_add_i32 s16, s29, 0x4000
	s_mov_b32 m0, s16
	s_nop 0
	global_load_lds_dwordx4 v1, s[18:19]
	s_add_i32 s20, s29, 0x6000
	s_mov_b32 m0, s20
	s_nop 0
	global_load_lds_dwordx4 v194, s[18:19]
	s_cmp_eq_u32 s15, 1
	s_mov_b32 s30, 0
	s_cselect_b64 s[16:17], -1, 0
	s_cmp_lg_u32 s15, 1
	s_cbranch_scc1 .LBB0_637
	s_barrier

; #define PG8_STAGE(bufoff, gbase, voff) do { PG8_GLDS((const char*)(gbase), (voff)[0], ldsb + (bufoff)); PG8_GLDS((const char*)(gbase), (voff)[1], ldsb + (bufoff) + 8192u); } while (0)
; #define PG8_STAGEA(bufoff, gbase, o0, o1) do { PG8_GLDS((const char*)(gbase), (o0), ldsb + (bufoff)); PG8_GLDS((const char*)(gbase), (o1), ldsb + (bufoff) + 8192u); } while (0)
; #define PG8_STAGEA1(bufoff, gbase) do { if constexpr (Sched::GATHER) { PG8_STAGEA(bufoff, gbase, vA2, vA3); } else { PG8_STAGEA(bufoff, (gbase) + hstep, vA0, vA1); } } while (0)
; #define PG8_LDA(dst, b, h) do { if constexpr (F8) { _Pragma("unroll") for (int m = 0; m < 4; ++m) dst##8[m] = PG8_LD32(lds + PG8_SA(b, h) + aoff + m * 2048); } else { \
;         _Pragma("unroll") for (int m = 0; m < 4; ++m) _Pragma("unroll") for (int k = 0; k < 2; ++k) dst[m][k] = *(const LAS bf16x8*)(lds + PG8_SA(b, h) + aoff + m * 2048 + k * 1024); } } while (0)
; #define PG8_LDB(dst, b, h) do { if constexpr (F8) { _Pragma("unroll") for (int n = 0; n < 2; ++n) dst##8[n] = PG8_LD32(lds + PG8_SB(b, h) + boff + n * 2048); } else { \
;         _Pragma("unroll") for (int n = 0; n < 2; ++n) _Pragma("unroll") for (int k = 0; k < 2; ++k) dst[n][k] = *(const LAS bf16x8*)(lds + PG8_SB(b, h) + boff + n * 2048 + k * 1024); } } while (0)
; template <class Epi, class Sched, bool F8 = false, bool PF = false, bool I8 = false, int PID = -1>
; __device__ __forceinline__ void gemm_phase(LAS unsigned char* lds, LAS unsigned char* xlds, const int RP, const int RPB, const int nt, const Sched& S, const Epi& E, const int stagger_ticks) {
;     ...
;             PG8_LDB(B0, 0, 0); PG8_LDB(B1, 0, 1); PG8_SCHED; PG8_LDA(At, 0, 0); PG8_STAGEA1(PG8_SA(1, 1), a1);
;             if (Sched::GATHER) { if (last) { const u32x4 nv = *nslot; vA0 = nv.x; vA1 = nv.y; vA2 = nv.z; vA3 = nv.w; } }
;             PG8_WAIT_VX(); PG8_WAIT_L(0); PG8_BAR; PG8_MMA(0, 0, At, B0); PG8_MMA(0, 1, At, B1); PG8_BAR; PG8_SCHED;
;             if constexpr (Epi::BIAS_DMA) { if (t == 0 && has_next) E.bias_dma(nxt, xlds + 8192 + ((ui + 1) & 1) * Epi::BIAS_STRIDE, wid, lane); }
;             PG8_LDA(At, 0, 1); PG8_STAGE(PG8_SB(0, 0), b2, voffB); PG8_STAGE(PG8_SB(0, 1), b2 + hstepB, voffB); PG8_STAGEA(PG8_SA(0, 0), a2, vA0, vA1);
;             PG8_WAIT_VX(); PG8_WAIT_L(0); PG8_BAR; PG8_MMA(1, 0, At, B0); PG8_MMA(1, 1, At, B1); PG8_BAR; PG8_SCHED;
.LBB0_640:
	s_mov_b64 s[24:25], s[10:11]
	s_add_u32 s42, s24, 0x100
	s_mov_b64 s[4:5], s[8:9]
	s_addc_u32 s43, s25, 0
	s_mov_b64 s[8:9], s[0:1]
	s_add_u32 s0, s4, 0x20080
	s_mov_b64 s[10:11], s[2:3]
	s_mov_b32 s15, s26
	s_mov_b32 s41, s6
	s_mov_b32 s6, s14
	s_mov_b32 s26, s7
	s_addc_u32 s1, s5, 0
	s_mov_b32 s44, -2
	s_mov_b32 s45, s29
	v_add_u32_e32 v131, 0x10000, v197
	ds_read_b128 v[132:135], v131
	ds_read_b128 v[136:139], v131 offset:1024
	ds_read_b128 v[140:143], v131 offset:2048
	ds_read_b128 v[144:147], v131 offset:3072
	v_add_u32_e32 v131, 0x14000, v197
	ds_read_b128 v[148:151], v131
	ds_read_b128 v[152:155], v131 offset:1024
	ds_read_b128 v[156:159], v131 offset:2048
	ds_read_b128 v[160:163], v131 offset:3072
	s_add_u32 s2, s0, 0xfffe0080
	s_addc_u32 s3, s1, -1
	s_cmp_eq_u32 s44, 4
	s_cselect_b32 s24, s8, s2
	s_cselect_b32 s25, s9, s3
	s_cselect_b32 s4, s10, s42
	s_cselect_b32 s5, s11, s43
	s_add_u32 s2, s24, 0x80
	s_addc_u32 s3, s25, 0
	ds_read_b128 v[164:167], v198
	ds_read_b128 v[168:171], v198 offset:1024
	ds_read_b128 v[172:175], v198 offset:2048
	ds_read_b128 v[176:179], v198 offset:3072
	ds_read_b128 v[180:183], v198 offset:4096
	ds_read_b128 v[184:187], v198 offset:5120
	ds_read_b128 v[202:205], v198 offset:6144
	ds_read_b128 v[206:209], v198 offset:7168
	s_add_i32 s46, s45, 0xc000
	s_mov_b32 m0, s46
	s_nop 0
	global_load_lds_dwordx4 v1, s[0:1]
	s_add_i32 s46, s45, 0xe000
	s_mov_b32 m0, s46
	s_nop 0
	global_load_lds_dwordx4 v194, s[0:1]
	s_waitcnt vmcnt(8)
	s_waitcnt lgkmcnt(0)
	s_barrier
	s_setprio 1
	s_waitcnt lgkmcnt(6)
	v_mfma_f32_16x16x128_f8f6f4 v[114:117], v[132:139], v[164:171], 0
	v_mfma_f32_16x16x128_f8f6f4 v[118:121], v[140:147], v[164:171], 0
	s_waitcnt lgkmcnt(4)
	v_mfma_f32_16x16x128_f8f6f4 v[102:105], v[132:139], v[172:179], 0
	v_mfma_f32_16x16x128_f8f6f4 v[98:101], v[140:147], v[172:179], 0
	s_waitcnt lgkmcnt(2)
	v_mfma_f32_16x16x128_f8f6f4 v[188:191], v[132:139], v[180:187], 0
	v_mfma_f32_16x16x128_f8f6f4 v[210:213], v[140:147], v[180:187], 0
	s_waitcnt lgkmcnt(0)
	v_mfma_f32_16x16x128_f8f6f4 v[214:217], v[132:139], v[202:209], 0
	v_mfma_f32_16x16x128_f8f6f4 v[218:221], v[140:147], v[202:209], 0
	s_setprio 0
	s_setprio 1
	v_mfma_f32_16x16x128_f8f6f4 v[122:125], v[148:155], v[164:171], 0
	v_mfma_f32_16x16x128_f8f6f4 v[126:129], v[156:163], v[164:171], 0
	v_mfma_f32_16x16x128_f8f6f4 v[110:113], v[148:155], v[172:179], 0
	v_mfma_f32_16x16x128_f8f6f4 v[106:109], v[156:163], v[172:179], 0
	v_mfma_f32_16x16x128_f8f6f4 v[164:167], v[148:155], v[180:187], 0
	v_mfma_f32_16x16x128_f8f6f4 v[168:171], v[156:163], v[180:187], 0
	v_mfma_f32_16x16x128_f8f6f4 v[172:175], v[148:155], v[202:209], 0
	v_mfma_f32_16x16x128_f8f6f4 v[176:179], v[156:163], v[202:209], 0
	s_setprio 0
	s_barrier
	ds_read_b128 v[66:69], v198 offset:16384
	ds_read_b128 v[70:73], v198 offset:17408
	s_nop 2
	ds_read_b128 v[74:77], v198 offset:18432
	ds_read_b128 v[78:81], v198 offset:19456
	ds_read_b128 v[82:85], v198 offset:20480
	ds_read_b128 v[86:89], v198 offset:21504
	ds_read_b128 v[90:93], v198 offset:22528
	ds_read_b128 v[94:97], v198 offset:23552
	s_add_i32 s46, s45, 0x10000
	s_mov_b32 m0, s46
	s_nop 0
	global_load_lds_dwordx4 v195, s[4:5]
	s_add_i32 s46, s45, 0x12000
	s_mov_b32 m0, s46
	s_nop 0
	global_load_lds_dwordx4 v196, s[4:5]
	s_add_u32 s46, s4, 0x2000
	s_addc_u32 s47, s5, 0
	s_add_i32 s48, s45, 0x14000
	s_mov_b32 m0, s48
	s_nop 0
	global_load_lds_dwordx4 v195, s[46:47]
	s_add_i32 s48, s45, 0x16000
	s_mov_b32 m0, s48
	s_nop 0
	global_load_lds_dwordx4 v196, s[46:47]
	s_add_i32 s46, s45, 0x2000
	s_mov_b32 m0, s45
	s_nop 0
	global_load_lds_dwordx4 v1, s[24:25]
	s_nop 0
	s_mov_b32 m0, s46
	s_nop 0
	global_load_lds_dwordx4 v194, s[24:25]
	s_waitcnt vmcnt(8)
	s_waitcnt lgkmcnt(0)
	s_barrier
	s_setprio 1
	s_waitcnt lgkmcnt(6)
	v_mfma_f32_16x16x128_f8f6f4 v[54:57], v[132:139], v[66:73], 0
	v_mfma_f32_16x16x128_f8f6f4 v[50:53], v[140:147], v[66:73], 0
	s_waitcnt lgkmcnt(4)
	v_mfma_f32_16x16x128_f8f6f4 v[180:183], v[132:139], v[74:81], 0
	v_mfma_f32_16x16x128_f8f6f4 v[184:187], v[140:147], v[74:81], 0
	s_waitcnt lgkmcnt(2)
	v_mfma_f32_16x16x128_f8f6f4 v[202:205], v[132:139], v[82:89], 0
	v_mfma_f32_16x16x128_f8f6f4 v[206:209], v[140:147], v[82:89], 0
	s_waitcnt lgkmcnt(0)
	v_mfma_f32_16x16x128_f8f6f4 v[222:225], v[132:139], v[90:97], 0
	v_mfma_f32_16x16x128_f8f6f4 v[226:229], v[140:147], v[90:97], 0
	s_setprio 0
	s_setprio 1
	v_mfma_f32_16x16x128_f8f6f4 v[62:65], v[148:155], v[66:73], 0
	v_mfma_f32_16x16x128_f8f6f4 v[58:61], v[156:163], v[66:73], 0
	v_mfma_f32_16x16x128_f8f6f4 v[230:233], v[148:155], v[74:81], 0
	v_mfma_f32_16x16x128_f8f6f4 v[234:237], v[156:163], v[74:81], 0
	v_mfma_f32_16x16x128_f8f6f4 v[238:241], v[148:155], v[82:89], 0
	v_mfma_f32_16x16x128_f8f6f4 v[242:245], v[156:163], v[82:89], 0
	v_mfma_f32_16x16x128_f8f6f4 v[246:249], v[148:155], v[90:97], 0
	v_mfma_f32_16x16x128_f8f6f4 v[250:253], v[156:163], v[90:97], 0
	s_setprio 0
	s_barrier
; #define PG8_STAGE(bufoff, gbase, voff) do { PG8_GLDS((const char*)(gbase), (voff)[0], ldsb + (bufoff)); PG8_GLDS((const char*)(gbase), (voff)[1], ldsb + (bufoff) + 8192u); } while (0)
; #define PG8_STAGEA(bufoff, gbase, o0, o1) do { PG8_GLDS((const char*)(gbase), (o0), ldsb + (bufoff)); PG8_GLDS((const char*)(gbase), (o1), ldsb + (bufoff) + 8192u); } while (0)
; #define PG8_STAGEA1(bufoff, gbase) do { if constexpr (Sched::GATHER) { PG8_STAGEA(bufoff, gbase, vA2, vA3); } else { PG8_STAGEA(bufoff, (gbase) + hstep, vA0, vA1); } } while (0)
; #define PG8_LDA(dst, b, h) do { if constexpr (F8) { _Pragma("unroll") for (int m = 0; m < 4; ++m) dst##8[m] = PG8_LD32(lds + PG8_SA(b, h) + aoff + m * 2048); } else { \
;         _Pragma("unroll") for (int m = 0; m < 4; ++m) _Pragma("unroll") for (int k = 0; k < 2; ++k) dst[m][k] = *(const LAS bf16x8*)(lds + PG8_SA(b, h) + aoff + m * 2048 + k * 1024); } } while (0)
; #define PG8_LDB(dst, b, h) do { if constexpr (F8) { _Pragma("unroll") for (int n = 0; n < 2; ++n) dst##8[n] = PG8_LD32(lds + PG8_SB(b, h) + boff + n * 2048); } else { \
;         _Pragma("unroll") for (int n = 0; n < 2; ++n) _Pragma("unroll") for (int k = 0; k < 2; ++k) dst[n][k] = *(const LAS bf16x8*)(lds + PG8_SB(b, h) + boff + n * 2048 + k * 1024); } } while (0)
; #define PG8_WAIT_VR() PG8_WAIT_V(8)
; #define PG8_WAIT_VX() do { if (relax) asm volatile("s_waitcnt vmcnt(%0)" :: "n"(8 + Epi::RELAX) : "memory"); else PG8_WAIT_V(8); } while (0)
; template <class Epi, class Sched, bool F8 = false, bool PF = false, bool I8 = false, int PID = -1>
; __device__ __forceinline__ void gemm_phase(LAS unsigned char* lds, LAS unsigned char* xlds, const int RP, const int RPB, const int nt, const Sched& S, const Epi& E, const int stagger_ticks) {
;     ...
;             PG8_WAIT_VX(); PG8_WAIT_L(0); PG8_BAR; PG8_MMA(1, 0, At, B0); PG8_MMA(1, 1, At, B1); PG8_BAR; PG8_SCHED;
;             PG8_LDB(B0, 1, 0); PG8_LDB(B1, 1, 1); PG8_SCHED; PG8_LDA(At, 1, 0); PG8_STAGEA1(PG8_SA(0, 1), a2);
;             PG8_WAIT_VR(); PG8_WAIT_L(0); PG8_BAR; PG8_MMA(0, 0, At, B0); PG8_MMA(0, 1, At, B1); PG8_BAR; PG8_SCHED;
;             PG8_LDA(At, 1, 1); PG8_STAGE(PG8_SB(1, 0), b3, voffB); PG8_STAGE(PG8_SB(1, 1), b3 + hstepB, voffB); PG8_STAGEA(PG8_SA(1, 0), a3, vA0, vA1);
;             PG8_WAIT_VR(); PG8_WAIT_L(0); PG8_BAR; PG8_MMA(1, 0, At, B0); PG8_MMA(1, 1, At, B1); PG8_BAR; PG8_SCHED;
;         }
	s_nop 3
	v_add_u32_e32 v14, 0x18000, v197
	v_add_u32_e32 v18, 0x1c000, v197
	ds_read_b128 v[2:5], v14
	ds_read_b128 v[6:9], v14 offset:1024
	ds_read_b128 v[10:13], v14 offset:2048
	ds_read_b128 v[14:17], v14 offset:3072
	ds_read_b128 v[132:135], v18
	ds_read_b128 v[136:139], v18 offset:1024
	ds_read_b128 v[140:143], v18 offset:2048
	ds_read_b128 v[144:147], v18 offset:3072
	ds_read_b128 v[18:21], v198 offset:32768
	ds_read_b128 v[22:25], v198 offset:33792
	ds_read_b128 v[26:29], v198 offset:34816
	ds_read_b128 v[30:33], v198 offset:35840
	ds_read_b128 v[34:37], v198 offset:36864
	ds_read_b128 v[38:41], v198 offset:37888
	ds_read_b128 v[42:45], v198 offset:38912
	ds_read_b128 v[46:49], v198 offset:39936
	s_add_u32 s24, s24, 0x20000
	s_addc_u32 s25, s25, 0
	s_add_i32 s46, s45, 0x4000
	s_mov_b32 m0, s46
	s_nop 0
	global_load_lds_dwordx4 v1, s[24:25]
	s_add_i32 s46, s45, 0x6000
	s_mov_b32 m0, s46
	s_nop 0
	global_load_lds_dwordx4 v194, s[24:25]
	s_waitcnt vmcnt(8)
	s_waitcnt lgkmcnt(0)
	s_barrier
	s_setprio 1
	s_waitcnt lgkmcnt(6)
	v_mfma_f32_16x16x128_f8f6f4 v[114:117], v[2:9], v[18:25], v[114:117]
	v_mfma_f32_16x16x128_f8f6f4 v[118:121], v[10:17], v[18:25], v[118:121]
	s_waitcnt lgkmcnt(4)
	v_mfma_f32_16x16x128_f8f6f4 v[102:105], v[2:9], v[26:33], v[102:105]
	v_mfma_f32_16x16x128_f8f6f4 v[98:101], v[10:17], v[26:33], v[98:101]
	s_waitcnt lgkmcnt(2)
	v_mfma_f32_16x16x128_f8f6f4 v[86:89], v[2:9], v[34:41], v[188:191]
	v_mfma_f32_16x16x128_f8f6f4 v[82:85], v[10:17], v[34:41], v[210:213]
	s_waitcnt lgkmcnt(0)
	v_mfma_f32_16x16x128_f8f6f4 v[70:73], v[2:9], v[42:49], v[214:217]
	v_mfma_f32_16x16x128_f8f6f4 v[66:69], v[10:17], v[42:49], v[218:221]
	s_setprio 0
	s_setprio 1
	v_mfma_f32_16x16x128_f8f6f4 v[122:125], v[132:139], v[18:25], v[122:125]
	v_mfma_f32_16x16x128_f8f6f4 v[126:129], v[140:147], v[18:25], v[126:129]
	v_mfma_f32_16x16x128_f8f6f4 v[110:113], v[132:139], v[26:33], v[110:113]
	v_mfma_f32_16x16x128_f8f6f4 v[106:109], v[140:147], v[26:33], v[106:109]
	v_mfma_f32_16x16x128_f8f6f4 v[94:97], v[132:139], v[34:41], v[164:167]
	v_mfma_f32_16x16x128_f8f6f4 v[90:93], v[140:147], v[34:41], v[168:171]
	v_mfma_f32_16x16x128_f8f6f4 v[78:81], v[132:139], v[42:49], v[172:175]
	v_mfma_f32_16x16x128_f8f6f4 v[74:77], v[140:147], v[42:49], v[176:179]
	s_setprio 0
	s_barrier
	s_add_u32 s24, s4, 0x80
	ds_read_b128 v[26:29], v198 offset:49152
	ds_read_b128 v[30:33], v198 offset:50176
	ds_read_b128 v[148:151], v198 offset:51200
	ds_read_b128 v[152:155], v198 offset:52224
	ds_read_b128 v[156:159], v198 offset:53248
	ds_read_b128 v[160:163], v198 offset:54272
	ds_read_b128 v[164:167], v198 offset:55296
	ds_read_b128 v[168:171], v198 offset:56320
	s_addc_u32 s25, s5, 0
	s_add_i32 s46, s45, 0x18000
	s_mov_b32 m0, s46
	s_nop 0
	global_load_lds_dwordx4 v195, s[24:25]
	s_add_i32 s46, s45, 0x1a000
	s_mov_b32 m0, s46
	s_nop 0
	global_load_lds_dwordx4 v196, s[24:25]
	s_add_u32 s4, s4, 0x2080
	s_addc_u32 s5, s5, 0
	s_add_i32 s24, s45, 0x1c000
	s_mov_b32 m0, s24
	s_nop 0
	global_load_lds_dwordx4 v195, s[4:5]
	s_add_i32 s24, s45, 0x1e000
	s_mov_b32 m0, s24
	s_nop 0
	global_load_lds_dwordx4 v196, s[4:5]
	s_add_i32 s4, s45, 0x8000
	s_mov_b32 m0, s4
	s_nop 0
	global_load_lds_dwordx4 v1, s[2:3]
	s_add_i32 s45, s45, 0xa000
	s_mov_b32 m0, s45
	s_nop 0
	global_load_lds_dwordx4 v194, s[2:3]
	s_waitcnt vmcnt(8)
	s_waitcnt lgkmcnt(0)
	s_barrier
	s_setprio 1
	s_waitcnt lgkmcnt(6)
	v_mfma_f32_16x16x128_f8f6f4 v[54:57], v[2:9], v[26:33], v[54:57]
	v_mfma_f32_16x16x128_f8f6f4 v[50:53], v[10:17], v[26:33], v[50:53]
	s_waitcnt lgkmcnt(4)
	v_mfma_f32_16x16x128_f8f6f4 v[38:41], v[2:9], v[148:155], v[180:183]
	v_mfma_f32_16x16x128_f8f6f4 v[34:37], v[10:17], v[148:155], v[184:187]
	s_waitcnt lgkmcnt(2)
	v_mfma_f32_16x16x128_f8f6f4 v[22:25], v[2:9], v[156:163], v[202:205]
	v_mfma_f32_16x16x128_f8f6f4 v[18:21], v[10:17], v[156:163], v[206:209]
	s_waitcnt lgkmcnt(0)
	v_mfma_f32_16x16x128_f8f6f4 v[6:9], v[2:9], v[164:171], v[222:225]
	v_mfma_f32_16x16x128_f8f6f4 v[2:5], v[10:17], v[164:171], v[226:229]
	s_setprio 0
	s_setprio 1
	v_mfma_f32_16x16x128_f8f6f4 v[62:65], v[132:139], v[26:33], v[62:65]
	v_mfma_f32_16x16x128_f8f6f4 v[58:61], v[140:147], v[26:33], v[58:61]
	v_mfma_f32_16x16x128_f8f6f4 v[46:49], v[132:139], v[148:155], v[230:233]
	v_mfma_f32_16x16x128_f8f6f4 v[42:45], v[140:147], v[148:155], v[234:237]
	v_mfma_f32_16x16x128_f8f6f4 v[30:33], v[132:139], v[156:163], v[238:241]
	v_mfma_f32_16x16x128_f8f6f4 v[26:29], v[140:147], v[156:163], v[242:245]
	v_mfma_f32_16x16x128_f8f6f4 v[14:17], v[132:139], v[164:171], v[246:249]
	v_mfma_f32_16x16x128_f8f6f4 v[10:13], v[140:147], v[164:171], v[250:253]
	s_setprio 0
	s_barrier
	s_add_i32 s44, s44, 2
	s_add_u32 s42, s42, 0x100
	s_addc_u32 s43, s43, 0
	s_add_u32 s0, s0, 0x100
	s_addc_u32 s1, s1, 0
	s_cmp_gt_u32 s44, 5

; #define PG8_UNI64(p) ((const char*)((((unsigned long long)(unsigned)__builtin_amdgcn_readfirstlane((int)((unsigned long long)(p) >> 32))) << 32) | (unsigned long long)(unsigned)__builtin_amdgcn_readfirstlane((int)(unsigned)(unsigned long long)(p))))
; #define PG8_BAR __builtin_amdgcn_s_barrier()
;     __device__ __forceinline__ const char* Abase(const pg8::Unit& u) const { size_t o = WS_R1; if (u.aux == 1) o = WS_R3; return ws + o + (size_t)u.pm * TSF8; }
;     __device__ __forceinline__ const char* Bbase(const pg8::Unit& u) const { size_t o = WS_WIN; if (u.aux == 1) o = WS_WKV; return ws + o + (size_t)u.pn * TSF8; }
;     __device__ __forceinline__ const char* Abase(const pg8::Unit& u) const { if (GATH) return ws + WS_XQ; return ws + WS_H2 + (size_t)u.pm * TSF8; }
; template <class Epi, class Sched, bool F8 = false, bool PF = false, bool I8 = false, int PID = -1>
; __device__ __forceinline__ void gemm_phase(LAS unsigned char* lds, LAS unsigned char* xlds, const int RP, const int RPB, const int nt, const Sched& S, const Epi& E, const int stagger_ticks) {
;     ...
;         cur = nxt; cA = nA; cB = nB; ++ui;
;         has_next = has_nn; nxt = nn;
;         if (has_next) { nA = PG8_UNI64(S.Abase(nxt)); nB = PG8_UNI64(S.Bbase(nxt)); }
;         if (Sched::GATHER) { *nslot = (u32x4){gv[0], gv[1], gv[2], gv[3]}; asm volatile("" ::: "memory"); }
;         PG8_ZERO_ACC();
;         if (wr == 1) PG8_BAR;
.LBB0_685:
	v_mov_b32_e32 v131, v130
	v_mov_b64_e32 v[132:133], v[130:131]
	s_andn2_b64 vcc, exec, s[16:17]
	s_cbranch_vccnz .LBB0_638
	s_barrier
	s_branch .LBB0_638

; #define PG8_STAGE(bufoff, gbase, voff) do { PG8_GLDS((const char*)(gbase), (voff)[0], ldsb + (bufoff)); PG8_GLDS((const char*)(gbase), (voff)[1], ldsb + (bufoff) + 8192u); } while (0)
; #define PG8_STAGEA(bufoff, gbase, o0, o1) do { PG8_GLDS((const char*)(gbase), (o0), ldsb + (bufoff)); PG8_GLDS((const char*)(gbase), (o1), ldsb + (bufoff) + 8192u); } while (0)
; #define PG8_STAGEA1(bufoff, gbase) do { if constexpr (Sched::GATHER) { PG8_STAGEA(bufoff, gbase, vA2, vA3); } else { PG8_STAGEA(bufoff, (gbase) + hstep, vA0, vA1); } } while (0)
; #define PG8_BAR __builtin_amdgcn_s_barrier()
; template <class Epi, class Sched, bool F8 = false, bool PF = false, bool I8 = false, int PID = -1>
; __device__ __forceinline__ void gemm_phase(LAS unsigned char* lds, LAS unsigned char* xlds, const int RP, const int RPB, const int nt, const Sched& S, const Epi& E, const int stagger_ticks) {
;     ...
;     for (int i = 0; i < 2; ++i) { int R, C; stage_rc(tid * 16 + i * 8192, R, C); Rr[i] = R; Cc[i] = C; const int Rb = Epi::PERM ? permB(R) : R; voffB[i] = (unsigned)(Rb * RPB + C * 2); }
;     const size_t kstep = (size_t)(BK * 2);
;     const size_t hstep = (size_t)HALF * RP, hstepB = (size_t)(Epi::PERM ? 8 : HALF) * RPB;
;     const unsigned ldsw = (unsigned)wid * 1024u;
;     const unsigned ldsb0 = (unsigned)__builtin_amdgcn_readfirstlane((int)(unsigned)(size_t)lds) + ldsw; const unsigned ldsb = ldsb0;
;     const int aoff = lds_byte(wr * 64 + fr, fq * 8), boff = lds_byte(wc * 32 + fr, fq * 8);
;     const unsigned voffP = (unsigned)((32 * wid + (lane & 31)) * RP + (lane >> 5) * 128);
;     ...
;     PG8_ZERO_ACC();
;     PG8_STAGE(PG8_SB(0, 0), cB, voffB); PG8_STAGE(PG8_SB(0, 1), cB + hstepB, voffB); PG8_STAGEA(PG8_SA(0, 0), cA, vA0, vA1); PG8_STAGEA1(PG8_SA(0, 1), cA);
;     if (wr == 1) PG8_BAR;
.LBB0_747:
	v_bfe_i32 v3, v130, 27, 1
	v_lshlrev_b32_e32 v1, 4, v130
	v_lshrrev_b32_e32 v3, 22, v3
	v_add_u32_e32 v3, v1, v3
	v_and_b32_e32 v3, 0xfffffc00, v3
	v_sub_u32_e32 v3, v1, v3
	v_lshrrev_b32_e32 v4, 4, v3
	v_bitop3_b32 v3, v4, v3, 32 bitop3:0x6c
	v_ashrrev_i32_e32 v5, 31, v3
	v_ashrrev_i32_e32 v2, 31, v130
	v_lshrrev_b32_e32 v5, 26, v5
	v_lshrrev_b32_e32 v2, 26, v2
	v_add_u32_e32 v5, v3, v5
	v_add_u32_e32 v2, v130, v2
	s_waitcnt vmcnt(6)
	v_ashrrev_i32_e32 v6, 6, v5
	v_and_b32_e32 v5, 0xc0, v5
	v_ashrrev_i32_e32 v2, 6, v2
	v_sub_u32_e32 v3, v3, v5
	v_mov_b32_e32 v5, 1
	v_lshlrev_b32_e32 v4, 3, v2
	v_lshlrev_b32_e32 v2, 5, v2
	v_ashrrev_i16_sdwa v3, v5, sext(v3) dst_sel:DWORD dst_unused:UNUSED_PAD src0_sel:DWORD src1_sel:BYTE_0
	v_and_b32_e32 v2, 32, v2
	v_bfe_i32 v3, v3, 0, 16
	v_add_u32_e32 v1, 0x2000, v1
	v_add_lshl_u32 v2, v2, v3, 1
	v_ashrrev_i32_e32 v3, 31, v1
	v_lshrrev_b32_e32 v3, 22, v3
	v_add_u32_e32 v3, v1, v3
	v_ashrrev_i32_e32 v3, 10, v3
	v_mul_i32_i24_e32 v7, 0x400, v3
	v_sub_u32_e32 v1, v1, v7
	v_lshrrev_b32_e32 v7, 4, v1
	v_bitop3_b32 v1, v7, v1, 32 bitop3:0x6c
	v_ashrrev_i32_e32 v8, 31, v1
	v_lshrrev_b32_e32 v8, 26, v8
	v_add_u32_e32 v8, v1, v8
	v_ashrrev_i32_e32 v9, 6, v8
	v_and_b32_e32 v8, 0xc0, v8
	v_sub_u32_e32 v1, v1, v8
	v_and_b32_e32 v4, -16, v4
	v_lshlrev_b32_e32 v7, 3, v3
	v_lshlrev_b32_e32 v3, 5, v3
	v_ashrrev_i16_sdwa v1, v5, sext(v1) dst_sel:DWORD dst_unused:UNUSED_PAD src0_sel:DWORD src1_sel:BYTE_0
	v_add_u32_e32 v4, v6, v4
	v_and_b32_e32 v3, 32, v3
	v_bfe_i32 v1, v1, 0, 16
	v_add_lshl_u32 v3, v3, v1, 1
	v_lshl_add_u32 v1, v4, 10, v2
	v_lshlrev_b32_e32 v5, 1, v4
	v_lshlrev_b32_e32 v8, 2, v4
	v_lshrrev_b32_e32 v4, 2, v4
	v_and_b32_e32 v6, 3, v6
	v_and_b32_e32 v7, -16, v7
	v_and_b32_e32 v5, 0x3fffc0, v5
	v_and_b32_e32 v4, 4, v4
	v_and_or_b32 v6, v8, 48, v6
	v_add_u32_e32 v7, v9, v7
	v_or3_b32 v4, v6, v5, v4
	s_ashr_i32 s13, s14, 6
	v_lshl_add_u32 v175, v4, 10, v2
	v_lshlrev_b32_e32 v2, 1, v7
	v_lshlrev_b32_e32 v4, 2, v7
	v_lshrrev_b32_e32 v5, 2, v7
	v_and_b32_e32 v6, 3, v9
	v_mov_b32_e32 v154, 0
	v_and_b32_e32 v2, 0x3fffc0, v2
	v_and_b32_e32 v5, 4, v5
	v_and_or_b32 v4, v4, 48, v6
	s_lshl_b32 s15, s13, 10
	v_mov_b32_e32 v155, v154
	v_or3_b32 v2, v4, v2, v5
	s_add_i32 s38, s15, 0
	v_mov_b64_e32 v[132:133], v[154:155]
	v_lshl_add_u32 v174, v7, 10, v3
	v_lshl_add_u32 v176, v2, 10, v3
	s_add_i32 s16, s38, 0x10000
	s_waitcnt vmcnt(0)
	s_ashr_i32 s24, s14, 8
	s_mov_b32 m0, s16
	s_nop 0
	global_load_lds_dwordx4 v175, s[8:9]
	s_add_i32 s16, s38, 0x12000
	s_mov_b32 m0, s16
	s_nop 0
	global_load_lds_dwordx4 v176, s[8:9]
	s_add_u32 s16, s8, 0x2000
	s_addc_u32 s17, s9, 0
	s_add_i32 s18, s38, 0x14000
	s_mov_b32 m0, s18
	s_nop 0
	global_load_lds_dwordx4 v175, s[16:17]
	s_add_i32 s18, s38, 0x16000
	s_mov_b32 m0, s18
	s_nop 0
	global_load_lds_dwordx4 v176, s[16:17]
	s_add_i32 s16, s38, 0x2000
	s_mov_b32 m0, s38
	s_nop 0
	global_load_lds_dwordx4 v1, s[6:7]
	s_add_u32 s18, s6, 0x20000
	s_mov_b32 m0, s16
	s_nop 0
	global_load_lds_dwordx4 v174, s[6:7]
	s_addc_u32 s19, s7, 0
	s_add_i32 s16, s38, 0x4000
	s_mov_b32 m0, s16
	s_nop 0
	global_load_lds_dwordx4 v1, s[18:19]
	s_add_i32 s20, s38, 0x6000
	s_mov_b32 m0, s20
	s_nop 0
	global_load_lds_dwordx4 v174, s[18:19]
	s_cmp_eq_u32 s24, 1
	s_mov_b32 s15, 0
	s_cselect_b64 s[16:17], -1, 0
	s_cmp_lg_u32 s24, 1
	s_cbranch_scc1 .LBB0_749
	s_barrier

; #define PG8_STAGE(bufoff, gbase, voff) do { PG8_GLDS((const char*)(gbase), (voff)[0], ldsb + (bufoff)); PG8_GLDS((const char*)(gbase), (voff)[1], ldsb + (bufoff) + 8192u); } while (0)
; #define PG8_STAGEA(bufoff, gbase, o0, o1) do { PG8_GLDS((const char*)(gbase), (o0), ldsb + (bufoff)); PG8_GLDS((const char*)(gbase), (o1), ldsb + (bufoff) + 8192u); } while (0)
; #define PG8_STAGEA1(bufoff, gbase) do { if constexpr (Sched::GATHER) { PG8_STAGEA(bufoff, gbase, vA2, vA3); } else { PG8_STAGEA(bufoff, (gbase) + hstep, vA0, vA1); } } while (0)
; #define PG8_LDA(dst, b, h) do { if constexpr (F8) { _Pragma("unroll") for (int m = 0; m < 4; ++m) dst##8[m] = PG8_LD32(lds + PG8_SA(b, h) + aoff + m * 2048); } else { \
;         _Pragma("unroll") for (int m = 0; m < 4; ++m) _Pragma("unroll") for (int k = 0; k < 2; ++k) dst[m][k] = *(const LAS bf16x8*)(lds + PG8_SA(b, h) + aoff + m * 2048 + k * 1024); } } while (0)
; #define PG8_LDB(dst, b, h) do { if constexpr (F8) { _Pragma("unroll") for (int n = 0; n < 2; ++n) dst##8[n] = PG8_LD32(lds + PG8_SB(b, h) + boff + n * 2048); } else { \
;         _Pragma("unroll") for (int n = 0; n < 2; ++n) _Pragma("unroll") for (int k = 0; k < 2; ++k) dst[n][k] = *(const LAS bf16x8*)(lds + PG8_SB(b, h) + boff + n * 2048 + k * 1024); } } while (0)
; template <class Epi, class Sched, bool F8 = false, bool PF = false, bool I8 = false, int PID = -1>
; __device__ __forceinline__ void gemm_phase(LAS unsigned char* lds, LAS unsigned char* xlds, const int RP, const int RPB, const int nt, const Sched& S, const Epi& E, const int stagger_ticks) {
;     ...
;             PG8_LDB(B0, 0, 0); PG8_LDB(B1, 0, 1); PG8_SCHED; PG8_LDA(At, 0, 0); PG8_STAGEA1(PG8_SA(1, 1), a1);
;             if (Sched::GATHER) { if (last) { const u32x4 nv = *nslot; vA0 = nv.x; vA1 = nv.y; vA2 = nv.z; vA3 = nv.w; } }
;             PG8_WAIT_VX(); PG8_WAIT_L(0); PG8_BAR; PG8_MMA(0, 0, At, B0); PG8_MMA(0, 1, At, B1); PG8_BAR; PG8_SCHED;
;             if constexpr (Epi::BIAS_DMA) { if (t == 0 && has_next) E.bias_dma(nxt, xlds + 8192 + ((ui + 1) & 1) * Epi::BIAS_STRIDE, wid, lane); }
;             PG8_LDA(At, 0, 1); PG8_STAGE(PG8_SB(0, 0), b2, voffB); PG8_STAGE(PG8_SB(0, 1), b2 + hstepB, voffB); PG8_STAGEA(PG8_SA(0, 0), a2, vA0, vA1);
;             PG8_WAIT_VX(); PG8_WAIT_L(0); PG8_BAR; PG8_MMA(1, 0, At, B0); PG8_MMA(1, 1, At, B1); PG8_BAR; PG8_SCHED;
.LBB0_752:
	s_mov_b64 s[30:31], s[8:9]
	s_add_u32 s43, s30, 0x100
	s_mov_b64 s[28:29], s[6:7]
	s_addc_u32 s44, s31, 0
	s_mov_b64 s[6:7], s[0:1]
	s_add_u32 s0, s28, 0x20080
	s_mov_b64 s[8:9], s[2:3]
	s_mov_b32 s13, s27
	s_mov_b32 s14, s4
	s_mov_b32 s4, s12
	s_mov_b32 s27, s5
	s_addc_u32 s1, s29, 0
	s_mov_b32 s45, -2
	s_mov_b32 s46, s38
	v_add_u32_e32 v142, 0x10000, v177
	v_add_u32_e32 v155, 0x14000, v177
	ds_read_b128 v[130:133], v142
	ds_read_b128 v[134:137], v142 offset:1024
	ds_read_b128 v[138:141], v142 offset:2048
	ds_read_b128 v[142:145], v142 offset:3072
	ds_read_b128 v[146:149], v155
	ds_read_b128 v[150:153], v155 offset:1024
	ds_read_b128 v[156:159], v155 offset:2048
	ds_read_b128 v[160:163], v155 offset:3072
	s_add_u32 s2, s0, 0xfffe0080
	s_addc_u32 s3, s1, -1
	s_cmp_eq_u32 s45, 4
	s_cselect_b32 s30, s6, s2
	s_cselect_b32 s31, s7, s3
	s_cselect_b32 s28, s8, s43
	s_cselect_b32 s29, s9, s44
	s_add_u32 s2, s30, 0x80
	s_addc_u32 s3, s31, 0
	ds_read_b128 v[164:167], v178
	ds_read_b128 v[168:171], v178 offset:1024
	ds_read_b128 v[180:183], v178 offset:2048
	ds_read_b128 v[184:187], v178 offset:3072
	ds_read_b128 v[188:191], v178 offset:4096
	ds_read_b128 v[192:195], v178 offset:5120
	ds_read_b128 v[196:199], v178 offset:6144
	ds_read_b128 v[200:203], v178 offset:7168
	s_add_i32 s47, s46, 0xc000
	s_mov_b32 m0, s47
	s_nop 0
	global_load_lds_dwordx4 v1, s[0:1]
	s_add_i32 s47, s46, 0xe000
	s_mov_b32 m0, s47
	s_nop 0
	global_load_lds_dwordx4 v174, s[0:1]
	s_waitcnt vmcnt(8)
	s_waitcnt lgkmcnt(0)
	s_barrier
	s_setprio 1
	s_waitcnt lgkmcnt(6)
	v_mfma_f32_16x16x128_f8f6f4 v[114:117], v[130:137], v[164:171], 0
	v_mfma_f32_16x16x128_f8f6f4 v[118:121], v[138:145], v[164:171], 0
	s_waitcnt lgkmcnt(4)
	v_mfma_f32_16x16x128_f8f6f4 v[110:113], v[130:137], v[180:187], 0
	v_mfma_f32_16x16x128_f8f6f4 v[106:109], v[138:145], v[180:187], 0
	s_waitcnt lgkmcnt(2)
	v_mfma_f32_16x16x128_f8f6f4 v[204:207], v[130:137], v[188:195], 0
	v_mfma_f32_16x16x128_f8f6f4 v[208:211], v[138:145], v[188:195], 0
	s_waitcnt lgkmcnt(0)
	v_mfma_f32_16x16x128_f8f6f4 v[212:215], v[130:137], v[196:203], 0
	v_mfma_f32_16x16x128_f8f6f4 v[216:219], v[138:145], v[196:203], 0
	s_setprio 0
	s_setprio 1
	v_mfma_f32_16x16x128_f8f6f4 v[122:125], v[146:153], v[164:171], 0
	v_mfma_f32_16x16x128_f8f6f4 v[126:129], v[156:163], v[164:171], 0
	v_mfma_f32_16x16x128_f8f6f4 v[102:105], v[146:153], v[180:187], 0
	v_mfma_f32_16x16x128_f8f6f4 v[98:101], v[156:163], v[180:187], 0
	v_mfma_f32_16x16x128_f8f6f4 v[164:167], v[146:153], v[188:195], 0
	v_mfma_f32_16x16x128_f8f6f4 v[168:171], v[156:163], v[188:195], 0
	v_mfma_f32_16x16x128_f8f6f4 v[180:183], v[146:153], v[196:203], 0
	v_mfma_f32_16x16x128_f8f6f4 v[184:187], v[156:163], v[196:203], 0
	s_setprio 0
	s_barrier
	s_nop 4
	ds_read_b128 v[66:69], v178 offset:16384
	ds_read_b128 v[70:73], v178 offset:17408
	ds_read_b128 v[74:77], v178 offset:18432
	ds_read_b128 v[78:81], v178 offset:19456
	ds_read_b128 v[82:85], v178 offset:20480
	ds_read_b128 v[86:89], v178 offset:21504
	ds_read_b128 v[90:93], v178 offset:22528
	ds_read_b128 v[94:97], v178 offset:23552
	s_add_i32 s47, s46, 0x10000
	s_mov_b32 m0, s47
	s_nop 0
	global_load_lds_dwordx4 v175, s[28:29]
	s_add_i32 s47, s46, 0x12000
	s_mov_b32 m0, s47
	s_nop 0
	global_load_lds_dwordx4 v176, s[28:29]
	s_add_u32 s48, s28, 0x2000
	s_addc_u32 s49, s29, 0
	s_add_i32 s47, s46, 0x14000
	s_mov_b32 m0, s47
	s_nop 0
	global_load_lds_dwordx4 v175, s[48:49]
	s_add_i32 s47, s46, 0x16000
	s_mov_b32 m0, s47
	s_nop 0
	global_load_lds_dwordx4 v176, s[48:49]
	s_add_i32 s47, s46, 0x2000
	s_mov_b32 m0, s46
	s_nop 0
	global_load_lds_dwordx4 v1, s[30:31]
	s_nop 0
	s_mov_b32 m0, s47
	s_nop 0
	global_load_lds_dwordx4 v174, s[30:31]
	s_waitcnt vmcnt(8)
	s_waitcnt lgkmcnt(0)
	s_barrier
	s_setprio 1
	s_waitcnt lgkmcnt(6)
	v_mfma_f32_16x16x128_f8f6f4 v[62:65], v[130:137], v[66:73], 0
	v_mfma_f32_16x16x128_f8f6f4 v[58:61], v[138:145], v[66:73], 0
	s_waitcnt lgkmcnt(4)
	v_mfma_f32_16x16x128_f8f6f4 v[188:191], v[130:137], v[74:81], 0
	v_mfma_f32_16x16x128_f8f6f4 v[192:195], v[138:145], v[74:81], 0
	s_waitcnt lgkmcnt(2)
	v_mfma_f32_16x16x128_f8f6f4 v[196:199], v[130:137], v[82:89], 0
	v_mfma_f32_16x16x128_f8f6f4 v[200:203], v[138:145], v[82:89], 0
	s_waitcnt lgkmcnt(0)
	v_mfma_f32_16x16x128_f8f6f4 v[220:223], v[130:137], v[90:97], 0
	v_mfma_f32_16x16x128_f8f6f4 v[224:227], v[138:145], v[90:97], 0
	s_setprio 0
	s_setprio 1
	v_mfma_f32_16x16x128_f8f6f4 v[54:57], v[146:153], v[66:73], 0
	v_mfma_f32_16x16x128_f8f6f4 v[50:53], v[156:163], v[66:73], 0
	v_mfma_f32_16x16x128_f8f6f4 v[228:231], v[146:153], v[74:81], 0
	v_mfma_f32_16x16x128_f8f6f4 v[232:235], v[156:163], v[74:81], 0
	v_mfma_f32_16x16x128_f8f6f4 v[236:239], v[146:153], v[82:89], 0
	v_mfma_f32_16x16x128_f8f6f4 v[240:243], v[156:163], v[82:89], 0
	v_mfma_f32_16x16x128_f8f6f4 v[244:247], v[146:153], v[90:97], 0
	v_mfma_f32_16x16x128_f8f6f4 v[248:251], v[156:163], v[90:97], 0
	s_setprio 0
	s_barrier
; #define PG8_STAGE(bufoff, gbase, voff) do { PG8_GLDS((const char*)(gbase), (voff)[0], ldsb + (bufoff)); PG8_GLDS((const char*)(gbase), (voff)[1], ldsb + (bufoff) + 8192u); } while (0)
; #define PG8_STAGEA(bufoff, gbase, o0, o1) do { PG8_GLDS((const char*)(gbase), (o0), ldsb + (bufoff)); PG8_GLDS((const char*)(gbase), (o1), ldsb + (bufoff) + 8192u); } while (0)
; #define PG8_STAGEA1(bufoff, gbase) do { if constexpr (Sched::GATHER) { PG8_STAGEA(bufoff, gbase, vA2, vA3); } else { PG8_STAGEA(bufoff, (gbase) + hstep, vA0, vA1); } } while (0)
; #define PG8_LDA(dst, b, h) do { if constexpr (F8) { _Pragma("unroll") for (int m = 0; m < 4; ++m) dst##8[m] = PG8_LD32(lds + PG8_SA(b, h) + aoff + m * 2048); } else { \
;         _Pragma("unroll") for (int m = 0; m < 4; ++m) _Pragma("unroll") for (int k = 0; k < 2; ++k) dst[m][k] = *(const LAS bf16x8*)(lds + PG8_SA(b, h) + aoff + m * 2048 + k * 1024); } } while (0)
; #define PG8_LDB(dst, b, h) do { if constexpr (F8) { _Pragma("unroll") for (int n = 0; n < 2; ++n) dst##8[n] = PG8_LD32(lds + PG8_SB(b, h) + boff + n * 2048); } else { \
;         _Pragma("unroll") for (int n = 0; n < 2; ++n) _Pragma("unroll") for (int k = 0; k < 2; ++k) dst[n][k] = *(const LAS bf16x8*)(lds + PG8_SB(b, h) + boff + n * 2048 + k * 1024); } } while (0)
; #define PG8_WAIT_VR() PG8_WAIT_V(8)
; #define PG8_WAIT_VX() do { if (relax) asm volatile("s_waitcnt vmcnt(%0)" :: "n"(8 + Epi::RELAX) : "memory"); else PG8_WAIT_V(8); } while (0)
; template <class Epi, class Sched, bool F8 = false, bool PF = false, bool I8 = false, int PID = -1>
; __device__ __forceinline__ void gemm_phase(LAS unsigned char* lds, LAS unsigned char* xlds, const int RP, const int RPB, const int nt, const Sched& S, const Epi& E, const int stagger_ticks) {
;     ...
;             PG8_WAIT_VX(); PG8_WAIT_L(0); PG8_BAR; PG8_MMA(1, 0, At, B0); PG8_MMA(1, 1, At, B1); PG8_BAR; PG8_SCHED;
;             PG8_LDB(B0, 1, 0); PG8_LDB(B1, 1, 1); PG8_SCHED; PG8_LDA(At, 1, 0); PG8_STAGEA1(PG8_SA(0, 1), a2);
;             PG8_WAIT_VR(); PG8_WAIT_L(0); PG8_BAR; PG8_MMA(0, 0, At, B0); PG8_MMA(0, 1, At, B1); PG8_BAR; PG8_SCHED;
;             PG8_LDA(At, 1, 1); PG8_STAGE(PG8_SB(1, 0), b3, voffB); PG8_STAGE(PG8_SB(1, 1), b3 + hstepB, voffB); PG8_STAGEA(PG8_SA(1, 0), a3, vA0, vA1);
;             PG8_WAIT_VR(); PG8_WAIT_L(0); PG8_BAR; PG8_MMA(1, 0, At, B0); PG8_MMA(1, 1, At, B1); PG8_BAR; PG8_SCHED;
;         }
	v_add_u32_e32 v10, 0x18000, v177
	s_nop 3
	ds_read_b128 v[2:5], v10
	ds_read_b128 v[6:9], v10 offset:1024
	ds_read_b128 v[18:21], v10 offset:2048
	ds_read_b128 v[22:25], v10 offset:3072
	v_add_u32_e32 v10, 0x1c000, v177
	ds_read_b128 v[130:133], v10
	ds_read_b128 v[134:137], v10 offset:1024
	ds_read_b128 v[138:141], v10 offset:2048
	ds_read_b128 v[142:145], v10 offset:3072
	ds_read_b128 v[10:13], v178 offset:32768
	ds_read_b128 v[14:17], v178 offset:33792
	ds_read_b128 v[26:29], v178 offset:34816
	ds_read_b128 v[30:33], v178 offset:35840
	ds_read_b128 v[34:37], v178 offset:36864
	ds_read_b128 v[38:41], v178 offset:37888
	ds_read_b128 v[42:45], v178 offset:38912
	ds_read_b128 v[46:49], v178 offset:39936
	s_add_u32 s30, s30, 0x20000
	s_addc_u32 s31, s31, 0
	s_add_i32 s47, s46, 0x4000
	s_mov_b32 m0, s47
	s_nop 0
	global_load_lds_dwordx4 v1, s[30:31]
	s_add_i32 s47, s46, 0x6000
	s_mov_b32 m0, s47
	s_nop 0
	global_load_lds_dwordx4 v174, s[30:31]
	s_waitcnt vmcnt(8)
	s_waitcnt lgkmcnt(0)
	s_barrier
	s_setprio 1
	s_waitcnt lgkmcnt(6)
	v_mfma_f32_16x16x128_f8f6f4 v[114:117], v[2:9], v[10:17], v[114:117]
	v_mfma_f32_16x16x128_f8f6f4 v[118:121], v[18:25], v[10:17], v[118:121]
	s_waitcnt lgkmcnt(4)
	v_mfma_f32_16x16x128_f8f6f4 v[110:113], v[2:9], v[26:33], v[110:113]
	v_mfma_f32_16x16x128_f8f6f4 v[106:109], v[18:25], v[26:33], v[106:109]
	s_waitcnt lgkmcnt(2)
	v_mfma_f32_16x16x128_f8f6f4 v[94:97], v[2:9], v[34:41], v[204:207]
	v_mfma_f32_16x16x128_f8f6f4 v[90:93], v[18:25], v[34:41], v[208:211]
	s_waitcnt lgkmcnt(0)
	v_mfma_f32_16x16x128_f8f6f4 v[78:81], v[2:9], v[42:49], v[212:215]
	v_mfma_f32_16x16x128_f8f6f4 v[74:77], v[18:25], v[42:49], v[216:219]
	s_setprio 0
	s_setprio 1
	v_mfma_f32_16x16x128_f8f6f4 v[122:125], v[130:137], v[10:17], v[122:125]
	v_mfma_f32_16x16x128_f8f6f4 v[126:129], v[138:145], v[10:17], v[126:129]
	v_mfma_f32_16x16x128_f8f6f4 v[102:105], v[130:137], v[26:33], v[102:105]
	v_mfma_f32_16x16x128_f8f6f4 v[98:101], v[138:145], v[26:33], v[98:101]
	v_mfma_f32_16x16x128_f8f6f4 v[86:89], v[130:137], v[34:41], v[164:167]
	v_mfma_f32_16x16x128_f8f6f4 v[82:85], v[138:145], v[34:41], v[168:171]
	v_mfma_f32_16x16x128_f8f6f4 v[70:73], v[130:137], v[42:49], v[180:183]
	v_mfma_f32_16x16x128_f8f6f4 v[66:69], v[138:145], v[42:49], v[184:187]
	s_setprio 0
	s_barrier
	s_add_u32 s30, s28, 0x80
	ds_read_b128 v[34:37], v178 offset:49152
	ds_read_b128 v[38:41], v178 offset:50176
	ds_read_b128 v[146:149], v178 offset:51200
	ds_read_b128 v[150:153], v178 offset:52224
	ds_read_b128 v[156:159], v178 offset:53248
	ds_read_b128 v[160:163], v178 offset:54272
	ds_read_b128 v[164:167], v178 offset:55296
	ds_read_b128 v[168:171], v178 offset:56320
	s_addc_u32 s31, s29, 0
	s_add_i32 s47, s46, 0x18000
	s_mov_b32 m0, s47
	s_nop 0
	global_load_lds_dwordx4 v175, s[30:31]
	s_add_i32 s47, s46, 0x1a000
	s_mov_b32 m0, s47
	s_nop 0
	global_load_lds_dwordx4 v176, s[30:31]
	s_add_u32 s28, s28, 0x2080
	s_addc_u32 s29, s29, 0
	s_add_i32 s30, s46, 0x1c000
	s_mov_b32 m0, s30
	s_nop 0
	global_load_lds_dwordx4 v175, s[28:29]
	s_add_i32 s30, s46, 0x1e000
	s_mov_b32 m0, s30
	s_nop 0
	global_load_lds_dwordx4 v176, s[28:29]
	s_add_i32 s28, s46, 0x8000
	s_mov_b32 m0, s28
	s_nop 0
	global_load_lds_dwordx4 v1, s[2:3]
	s_add_i32 s46, s46, 0xa000
	s_mov_b32 m0, s46
	s_nop 0
	global_load_lds_dwordx4 v174, s[2:3]
	s_waitcnt vmcnt(8)
	s_waitcnt lgkmcnt(0)
	s_barrier
	s_setprio 1
	s_waitcnt lgkmcnt(6)
	v_mfma_f32_16x16x128_f8f6f4 v[62:65], v[2:9], v[34:41], v[62:65]
	v_mfma_f32_16x16x128_f8f6f4 v[58:61], v[18:25], v[34:41], v[58:61]
	s_waitcnt lgkmcnt(4)
	v_mfma_f32_16x16x128_f8f6f4 v[46:49], v[2:9], v[146:153], v[188:191]
	v_mfma_f32_16x16x128_f8f6f4 v[42:45], v[18:25], v[146:153], v[192:195]
	s_waitcnt lgkmcnt(2)
	v_mfma_f32_16x16x128_f8f6f4 v[30:33], v[2:9], v[156:163], v[196:199]
	v_mfma_f32_16x16x128_f8f6f4 v[26:29], v[18:25], v[156:163], v[200:203]
	s_waitcnt lgkmcnt(0)
	v_mfma_f32_16x16x128_f8f6f4 v[14:17], v[2:9], v[164:171], v[220:223]
	v_mfma_f32_16x16x128_f8f6f4 v[10:13], v[18:25], v[164:171], v[224:227]
	s_setprio 0
	s_setprio 1
	v_mfma_f32_16x16x128_f8f6f4 v[54:57], v[130:137], v[34:41], v[54:57]
	v_mfma_f32_16x16x128_f8f6f4 v[50:53], v[138:145], v[34:41], v[50:53]
	v_mfma_f32_16x16x128_f8f6f4 v[38:41], v[130:137], v[146:153], v[228:231]
	v_mfma_f32_16x16x128_f8f6f4 v[34:37], v[138:145], v[146:153], v[232:235]
	v_mfma_f32_16x16x128_f8f6f4 v[22:25], v[130:137], v[156:163], v[236:239]
	v_mfma_f32_16x16x128_f8f6f4 v[18:21], v[138:145], v[156:163], v[240:243]
	v_mfma_f32_16x16x128_f8f6f4 v[6:9], v[130:137], v[164:171], v[244:247]
	v_mfma_f32_16x16x128_f8f6f4 v[2:5], v[138:145], v[164:171], v[248:251]
	s_setprio 0
	s_barrier
	s_add_i32 s45, s45, 2
	s_add_u32 s43, s43, 0x100
	s_addc_u32 s44, s44, 0
	s_add_u32 s0, s0, 0x100
	s_addc_u32 s1, s1, 0
	s_cmp_gt_u32 s45, 5

; #define PG8_UNI64(p) ((const char*)((((unsigned long long)(unsigned)__builtin_amdgcn_readfirstlane((int)((unsigned long long)(p) >> 32))) << 32) | (unsigned long long)(unsigned)__builtin_amdgcn_readfirstlane((int)(unsigned)(unsigned long long)(p))))
; #define PG8_BAR __builtin_amdgcn_s_barrier()
;     __device__ __forceinline__ const char* Abase(const pg8::Unit& u) const { size_t o = WS_R1; if (u.aux == 1) o = WS_R3; return ws + o + (size_t)u.pm * TSF8; }
;     __device__ __forceinline__ const char* Bbase(const pg8::Unit& u) const { size_t o = WS_WIN; if (u.aux == 1) o = WS_WKV; return ws + o + (size_t)u.pn * TSF8; }
;     __device__ __forceinline__ const char* Abase(const pg8::Unit& u) const { if (GATH) return ws + WS_XQ; return ws + WS_H2 + (size_t)u.pm * TSF8; }
; template <class Epi, class Sched, bool F8 = false, bool PF = false, bool I8 = false, int PID = -1>
; __device__ __forceinline__ void gemm_phase(LAS unsigned char* lds, LAS unsigned char* xlds, const int RP, const int RPB, const int nt, const Sched& S, const Epi& E, const int stagger_ticks) {
;     ...
;         cur = nxt; cA = nA; cB = nB; ++ui;
;         has_next = has_nn; nxt = nn;
;         if (has_next) { nA = PG8_UNI64(S.Abase(nxt)); nB = PG8_UNI64(S.Bbase(nxt)); }
;         if (Sched::GATHER) { *nslot = (u32x4){gv[0], gv[1], gv[2], gv[3]}; asm volatile("" ::: "memory"); }
;         PG8_ZERO_ACC();
;         if (wr == 1) PG8_BAR;
.LBB0_779:
	v_mov_b32_e32 v155, v154
	v_mov_b64_e32 v[130:131], v[154:155]
	s_andn2_b64 vcc, exec, s[16:17]
	s_waitcnt lgkmcnt(0)
	s_cbranch_vccnz .LBB0_750
	s_barrier
	s_branch .LBB0_750

; #define PG8_STAGE(bufoff, gbase, voff) do { PG8_GLDS((const char*)(gbase), (voff)[0], ldsb + (bufoff)); PG8_GLDS((const char*)(gbase), (voff)[1], ldsb + (bufoff) + 8192u); } while (0)
; #define PG8_STAGEA(bufoff, gbase, o0, o1) do { PG8_GLDS((const char*)(gbase), (o0), ldsb + (bufoff)); PG8_GLDS((const char*)(gbase), (o1), ldsb + (bufoff) + 8192u); } while (0)
; #define PG8_STAGEA1(bufoff, gbase) do { if constexpr (Sched::GATHER) { PG8_STAGEA(bufoff, gbase, vA2, vA3); } else { PG8_STAGEA(bufoff, (gbase) + hstep, vA0, vA1); } } while (0)
; #define PG8_BAR __builtin_amdgcn_s_barrier()
; template <class Epi, class Sched, bool F8 = false, bool PF = false, bool I8 = false, int PID = -1>
; __device__ __forceinline__ void gemm_phase(LAS unsigned char* lds, LAS unsigned char* xlds, const int RP, const int RPB, const int nt, const Sched& S, const Epi& E, const int stagger_ticks) {
;     ...
;     for (int i = 0; i < 2; ++i) { int R, C; stage_rc(tid * 16 + i * 8192, R, C); Rr[i] = R; Cc[i] = C; const int Rb = Epi::PERM ? permB(R) : R; voffB[i] = (unsigned)(Rb * RPB + C * 2); }
;     const size_t kstep = (size_t)(BK * 2);
;     const size_t hstep = (size_t)HALF * RP, hstepB = (size_t)(Epi::PERM ? 8 : HALF) * RPB;
;     const unsigned ldsw = (unsigned)wid * 1024u;
;     const unsigned ldsb0 = (unsigned)__builtin_amdgcn_readfirstlane((int)(unsigned)(size_t)lds) + ldsw; const unsigned ldsb = ldsb0;
;     const int aoff = lds_byte(wr * 64 + fr, fq * 8), boff = lds_byte(wc * 32 + fr, fq * 8);
;     const unsigned voffP = (unsigned)((32 * wid + (lane & 31)) * RP + (lane >> 5) * 128);
;     ...
;     PG8_ZERO_ACC();
;     PG8_STAGE(PG8_SB(0, 0), cB, voffB); PG8_STAGE(PG8_SB(0, 1), cB + hstepB, voffB); PG8_STAGEA(PG8_SA(0, 0), cA, vA0, vA1); PG8_STAGEA1(PG8_SA(0, 1), cA);
;     if (wr == 1) PG8_BAR;
.LBB0_1056:
	v_bfe_i32 v5, v2, 27, 1
	v_lshlrev_b32_e32 v3, 4, v2
	v_lshrrev_b32_e32 v5, 22, v5
	v_add_u32_e32 v5, v3, v5
	v_and_b32_e32 v5, 0xfffffc00, v5
	v_sub_u32_e32 v5, v3, v5
	v_lshrrev_b32_e32 v6, 4, v5
	v_bitop3_b32 v5, v6, v5, 32 bitop3:0x6c
	v_ashrrev_i32_e32 v7, 31, v5
	v_ashrrev_i32_e32 v4, 31, v2
	v_lshrrev_b32_e32 v7, 26, v7
	v_lshrrev_b32_e32 v4, 26, v4
	v_add_u32_e32 v7, v5, v7
	v_add_u32_e32 v4, v2, v4
	v_ashrrev_i32_e32 v8, 6, v7
	v_and_b32_e32 v7, 0xc0, v7
	v_ashrrev_i32_e32 v4, 6, v4
	v_sub_u32_e32 v5, v5, v7
	v_mov_b32_e32 v7, 1
	v_lshlrev_b32_e32 v6, 3, v4
	v_lshlrev_b32_e32 v4, 5, v4
	v_ashrrev_i16_sdwa v5, v7, sext(v5) dst_sel:DWORD dst_unused:UNUSED_PAD src0_sel:DWORD src1_sel:BYTE_0
	v_and_b32_e32 v4, 32, v4
	v_bfe_i32 v5, v5, 0, 16
	v_add_u32_e32 v3, 0x2000, v3
	v_add_lshl_u32 v4, v4, v5, 1
	v_ashrrev_i32_e32 v5, 31, v3
	v_lshrrev_b32_e32 v5, 22, v5
	v_add_u32_e32 v5, v3, v5
	v_ashrrev_i32_e32 v5, 10, v5
	v_mul_i32_i24_e32 v9, 0x400, v5
	v_sub_u32_e32 v3, v3, v9
	v_lshrrev_b32_e32 v9, 4, v3
	v_bitop3_b32 v3, v9, v3, 32 bitop3:0x6c
	v_ashrrev_i32_e32 v10, 31, v3
	v_lshrrev_b32_e32 v10, 26, v10
	v_add_u32_e32 v10, v3, v10
	v_ashrrev_i32_e32 v11, 6, v10
	v_and_b32_e32 v10, 0xc0, v10
	v_sub_u32_e32 v3, v3, v10
	v_and_b32_e32 v6, -16, v6
	v_lshlrev_b32_e32 v9, 3, v5
	v_lshlrev_b32_e32 v5, 5, v5
	v_ashrrev_i16_sdwa v3, v7, sext(v3) dst_sel:DWORD dst_unused:UNUSED_PAD src0_sel:DWORD src1_sel:BYTE_0
	v_add_u32_e32 v6, v8, v6
	v_and_b32_e32 v5, 32, v5
	v_bfe_i32 v3, v3, 0, 16
	v_add_lshl_u32 v3, v5, v3, 1
	v_lshl_add_u32 v164, v6, 10, v4
	v_lshlrev_b32_e32 v5, 1, v6
	v_lshlrev_b32_e32 v7, 2, v6
	v_lshrrev_b32_e32 v6, 2, v6
	v_and_b32_e32 v8, 3, v8
	v_and_b32_e32 v9, -16, v9
	v_and_b32_e32 v5, 0x3fffc0, v5
	v_and_b32_e32 v6, 4, v6
	v_and_or_b32 v7, v7, 48, v8
	v_add_u32_e32 v9, v11, v9
	v_or3_b32 v5, v7, v5, v6
	v_lshl_add_u32 v166, v5, 10, v4
	v_lshlrev_b32_e32 v4, 1, v9
	v_lshlrev_b32_e32 v5, 2, v9
	v_lshrrev_b32_e32 v6, 2, v9
	v_and_b32_e32 v7, 3, v11
	v_and_b32_e32 v4, 0x3fffc0, v4
	v_and_b32_e32 v6, 4, v6
	v_and_or_b32 v5, v5, 48, v7
	v_mov_b32_e32 v162, 0
	v_or3_b32 v4, v5, v4, v6
	s_lshl_b32 s16, s19, 10
	v_mov_b32_e32 v163, v162
	v_lshl_add_u32 v167, v4, 10, v3
	s_add_i32 s47, s16, 0
	v_mov_b64_e32 v[4:5], v[162:163]
	s_add_i32 s16, s47, 0x10000
	s_ashr_i32 s15, s18, 8
	s_mov_b32 m0, s16
	s_nop 0
	global_load_lds_dwordx4 v166, s[8:9]
	s_add_i32 s16, s47, 0x12000
	s_mov_b32 m0, s16
	s_nop 0
	global_load_lds_dwordx4 v167, s[8:9]
	s_add_u32 s16, s8, 0x2000
	s_addc_u32 s17, s9, 0
	s_add_i32 s20, s47, 0x14000
	s_mov_b32 m0, s20
	s_nop 0
	global_load_lds_dwordx4 v166, s[16:17]
	s_add_i32 s20, s47, 0x16000
	s_mov_b32 m0, s20
	s_nop 0
	global_load_lds_dwordx4 v167, s[16:17]
	s_add_i32 s16, s47, 0x2000
	s_mov_b32 m0, s47
	s_nop 0
	global_load_lds_dwordx4 v164, s[6:7]
	v_lshl_add_u32 v165, v9, 10, v3
	s_mov_b32 m0, s16
	s_nop 0
	global_load_lds_dwordx4 v165, s[6:7]
	s_add_u32 s20, s6, 0x20000
	s_addc_u32 s21, s7, 0
	s_add_i32 s16, s47, 0x4000
	s_mov_b32 m0, s16
	s_nop 0
	global_load_lds_dwordx4 v164, s[20:21]
	s_add_i32 s22, s47, 0x6000
	s_mov_b32 m0, s22
	s_nop 0
	global_load_lds_dwordx4 v165, s[20:21]
	s_cmp_eq_u32 s15, 1
	s_mov_b32 s48, 0
	s_cselect_b64 s[16:17], -1, 0
	s_cmp_lg_u32 s15, 1
	s_cbranch_scc1 .LBB0_1058
	s_barrier

; #define PG8_STAGE(bufoff, gbase, voff) do { PG8_GLDS((const char*)(gbase), (voff)[0], ldsb + (bufoff)); PG8_GLDS((const char*)(gbase), (voff)[1], ldsb + (bufoff) + 8192u); } while (0)
; #define PG8_STAGEA(bufoff, gbase, o0, o1) do { PG8_GLDS((const char*)(gbase), (o0), ldsb + (bufoff)); PG8_GLDS((const char*)(gbase), (o1), ldsb + (bufoff) + 8192u); } while (0)
; #define PG8_STAGEA1(bufoff, gbase) do { if constexpr (Sched::GATHER) { PG8_STAGEA(bufoff, gbase, vA2, vA3); } else { PG8_STAGEA(bufoff, (gbase) + hstep, vA0, vA1); } } while (0)
; #define PG8_LDA(dst, b, h) do { if constexpr (F8) { _Pragma("unroll") for (int m = 0; m < 4; ++m) dst##8[m] = PG8_LD32(lds + PG8_SA(b, h) + aoff + m * 2048); } else { \
;         _Pragma("unroll") for (int m = 0; m < 4; ++m) _Pragma("unroll") for (int k = 0; k < 2; ++k) dst[m][k] = *(const LAS bf16x8*)(lds + PG8_SA(b, h) + aoff + m * 2048 + k * 1024); } } while (0)
; #define PG8_LDB(dst, b, h) do { if constexpr (F8) { _Pragma("unroll") for (int n = 0; n < 2; ++n) dst##8[n] = PG8_LD32(lds + PG8_SB(b, h) + boff + n * 2048); } else { \
;         _Pragma("unroll") for (int n = 0; n < 2; ++n) _Pragma("unroll") for (int k = 0; k < 2; ++k) dst[n][k] = *(const LAS bf16x8*)(lds + PG8_SB(b, h) + boff + n * 2048 + k * 1024); } } while (0)
; template <class Epi, class Sched, bool F8 = false, bool PF = false, bool I8 = false, int PID = -1>
; __device__ __forceinline__ void gemm_phase(LAS unsigned char* lds, LAS unsigned char* xlds, const int RP, const int RPB, const int nt, const Sched& S, const Epi& E, const int stagger_ticks) {
;     ...
;             PG8_LDB(B0, 0, 0); PG8_LDB(B1, 0, 1); PG8_SCHED; PG8_LDA(At, 0, 0); PG8_STAGEA1(PG8_SA(1, 1), a1);
;             if (Sched::GATHER) { if (last) { const u32x4 nv = *nslot; vA0 = nv.x; vA1 = nv.y; vA2 = nv.z; vA3 = nv.w; } }
;             PG8_WAIT_VX(); PG8_WAIT_L(0); PG8_BAR; PG8_MMA(0, 0, At, B0); PG8_MMA(0, 1, At, B1); PG8_BAR; PG8_SCHED;
;             if constexpr (Epi::BIAS_DMA) { if (t == 0 && has_next) E.bias_dma(nxt, xlds + 8192 + ((ui + 1) & 1) * Epi::BIAS_STRIDE, wid, lane); }
;             PG8_LDA(At, 0, 1); PG8_STAGE(PG8_SB(0, 0), b2, voffB); PG8_STAGE(PG8_SB(0, 1), b2 + hstepB, voffB); PG8_STAGEA(PG8_SA(0, 0), a2, vA0, vA1);
;             PG8_WAIT_VX(); PG8_WAIT_L(0); PG8_BAR; PG8_MMA(1, 0, At, B0); PG8_MMA(1, 1, At, B1); PG8_BAR; PG8_SCHED;
.Lmy_z8t:
	s_mov_b32 s74, s47
	v_add_u32_e32 v14, 0x10000, v168
	v_add_u32_e32 v30, 0x14000, v168
	ds_read_b128 v[2:5], v14
	ds_read_b128 v[6:9], v14 offset:1024
	ds_read_b128 v[10:13], v14 offset:2048
	ds_read_b128 v[14:17], v14 offset:3072
	ds_read_b128 v[18:21], v30
	ds_read_b128 v[22:25], v30 offset:1024
	ds_read_b128 v[26:29], v30 offset:2048
	ds_read_b128 v[30:33], v30 offset:3072
	ds_read_b128 v[170:173], v169
	ds_read_b128 v[174:177], v169 offset:1024
	ds_read_b128 v[178:181], v169 offset:2048
	ds_read_b128 v[182:185], v169 offset:3072
	ds_read_b128 v[186:189], v169 offset:4096
	ds_read_b128 v[190:193], v169 offset:5120
	ds_read_b128 v[194:197], v169 offset:6144
	ds_read_b128 v[198:201], v169 offset:7168
	s_add_i32 s30, s74, 0xc000
	s_mov_b32 m0, s30
	s_nop 0
	global_load_lds_dwordx4 v164, s[26:27]
	s_add_i32 s30, s74, 0xe000
	s_mov_b32 m0, s30
	s_nop 0
	global_load_lds_dwordx4 v165, s[26:27]
	s_waitcnt vmcnt(8)
	s_waitcnt lgkmcnt(0)
	s_barrier
	s_setprio 1
	s_waitcnt lgkmcnt(6)
	v_mfma_f32_16x16x128_f8f6f4 v[150:153], v[2:9], v[170:177], 0
	v_mfma_f32_16x16x128_f8f6f4 v[146:149], v[10:17], v[170:177], 0
	s_waitcnt lgkmcnt(4)
	v_mfma_f32_16x16x128_f8f6f4 v[134:137], v[2:9], v[178:185], 0
	v_mfma_f32_16x16x128_f8f6f4 v[130:133], v[10:17], v[178:185], 0
	s_waitcnt lgkmcnt(2)
	v_mfma_f32_16x16x128_f8f6f4 v[118:121], v[2:9], v[186:193], 0
	v_mfma_f32_16x16x128_f8f6f4 v[114:117], v[10:17], v[186:193], 0
	s_waitcnt lgkmcnt(0)
	v_mfma_f32_16x16x128_f8f6f4 v[102:105], v[2:9], v[194:201], 0
	v_mfma_f32_16x16x128_f8f6f4 v[98:101], v[10:17], v[194:201], 0
	s_setprio 0
	s_setprio 1
	v_mfma_f32_16x16x128_f8f6f4 v[158:161], v[18:25], v[170:177], 0
	v_mfma_f32_16x16x128_f8f6f4 v[154:157], v[26:33], v[170:177], 0
	v_mfma_f32_16x16x128_f8f6f4 v[142:145], v[18:25], v[178:185], 0
	v_mfma_f32_16x16x128_f8f6f4 v[138:141], v[26:33], v[178:185], 0
	v_mfma_f32_16x16x128_f8f6f4 v[126:129], v[18:25], v[186:193], 0
	v_mfma_f32_16x16x128_f8f6f4 v[122:125], v[26:33], v[186:193], 0
	v_mfma_f32_16x16x128_f8f6f4 v[110:113], v[18:25], v[194:201], 0
	v_mfma_f32_16x16x128_f8f6f4 v[106:109], v[26:33], v[194:201], 0
	s_setprio 0
	s_barrier
	s_cmp_lg_u32 s73, -2
	s_cselect_b64 s[30:31], -1, 0
	s_or_b64 s[30:31], s[30:31], s[28:29]
	s_and_b64 vcc, exec, s[30:31]
	s_cbranch_vccnz .Lmy_z8b
	s_mov_b32 m0, s72
	s_nop 0
	global_load_lds_dword v1, s[2:3]
	s_branch .Lmy_z8b
.Lmy_z8b:
	s_add_u32 s30, s26, 0xfffe0080
	s_addc_u32 s31, s27, -1
	s_cmp_eq_u32 s73, 4
	s_cselect_b32 s38, s6, s30
	s_cselect_b32 s39, s7, s31
	s_cselect_b32 s34, s8, s25
	s_cselect_b32 s35, s9, s71
	s_add_u32 s30, s38, 0x80
	s_addc_u32 s31, s39, 0
	s_add_u32 s36, s34, 0x80
	s_addc_u32 s37, s35, 0
	ds_read_b128 v[170:173], v169 offset:16384
	ds_read_b128 v[174:177], v169 offset:17408
	ds_read_b128 v[178:181], v169 offset:18432
	ds_read_b128 v[182:185], v169 offset:19456
	ds_read_b128 v[186:189], v169 offset:20480
	ds_read_b128 v[190:193], v169 offset:21504
	ds_read_b128 v[194:197], v169 offset:22528
	ds_read_b128 v[198:201], v169 offset:23552
	s_add_i32 s75, s74, 0x10000
	s_mov_b32 m0, s75
	s_nop 0
	global_load_lds_dwordx4 v166, s[34:35]
	s_add_i32 s75, s74, 0x12000
	s_mov_b32 m0, s75
	s_nop 0
	global_load_lds_dwordx4 v167, s[34:35]
	s_add_u32 s76, s34, 0x2000
	s_addc_u32 s77, s35, 0
	s_add_i32 s75, s74, 0x14000
	s_mov_b32 m0, s75
	s_nop 0
	global_load_lds_dwordx4 v166, s[76:77]
	s_add_i32 s75, s74, 0x16000
	s_mov_b32 m0, s75
	s_nop 0
	global_load_lds_dwordx4 v167, s[76:77]
	s_add_i32 s75, s74, 0x2000
	s_mov_b32 m0, s74
	s_nop 0
	global_load_lds_dwordx4 v164, s[38:39]
	s_nop 0
	s_mov_b32 m0, s75
	s_nop 0
	global_load_lds_dwordx4 v165, s[38:39]
	s_waitcnt vmcnt(8)
	s_waitcnt lgkmcnt(0)
	s_barrier
	s_setprio 1
	s_waitcnt lgkmcnt(6)
	v_mfma_f32_16x16x128_f8f6f4 v[86:89], v[2:9], v[170:177], 0
	v_mfma_f32_16x16x128_f8f6f4 v[82:85], v[10:17], v[170:177], 0
	s_waitcnt lgkmcnt(4)
	v_mfma_f32_16x16x128_f8f6f4 v[70:73], v[2:9], v[178:185], 0
	v_mfma_f32_16x16x128_f8f6f4 v[66:69], v[10:17], v[178:185], 0
	s_waitcnt lgkmcnt(2)
	v_mfma_f32_16x16x128_f8f6f4 v[202:205], v[2:9], v[186:193], 0
	v_mfma_f32_16x16x128_f8f6f4 v[206:209], v[10:17], v[186:193], 0
	s_waitcnt lgkmcnt(0)
	v_mfma_f32_16x16x128_f8f6f4 v[210:213], v[2:9], v[194:201], 0
	v_mfma_f32_16x16x128_f8f6f4 v[214:217], v[10:17], v[194:201], 0
	s_setprio 0
	s_setprio 1
	v_mfma_f32_16x16x128_f8f6f4 v[94:97], v[18:25], v[170:177], 0
	v_mfma_f32_16x16x128_f8f6f4 v[90:93], v[26:33], v[170:177], 0
	v_mfma_f32_16x16x128_f8f6f4 v[78:81], v[18:25], v[178:185], 0
	v_mfma_f32_16x16x128_f8f6f4 v[74:77], v[26:33], v[178:185], 0
	v_mfma_f32_16x16x128_f8f6f4 v[218:221], v[18:25], v[186:193], 0
	v_mfma_f32_16x16x128_f8f6f4 v[186:189], v[26:33], v[186:193], 0
	v_mfma_f32_16x16x128_f8f6f4 v[190:193], v[18:25], v[194:201], 0
	v_mfma_f32_16x16x128_f8f6f4 v[194:197], v[26:33], v[194:201], 0
	s_setprio 0
	s_barrier
; #define PG8_STAGE(bufoff, gbase, voff) do { PG8_GLDS((const char*)(gbase), (voff)[0], ldsb + (bufoff)); PG8_GLDS((const char*)(gbase), (voff)[1], ldsb + (bufoff) + 8192u); } while (0)
; #define PG8_STAGEA(bufoff, gbase, o0, o1) do { PG8_GLDS((const char*)(gbase), (o0), ldsb + (bufoff)); PG8_GLDS((const char*)(gbase), (o1), ldsb + (bufoff) + 8192u); } while (0)
; #define PG8_STAGEA1(bufoff, gbase) do { if constexpr (Sched::GATHER) { PG8_STAGEA(bufoff, gbase, vA2, vA3); } else { PG8_STAGEA(bufoff, (gbase) + hstep, vA0, vA1); } } while (0)
; #define PG8_LDA(dst, b, h) do { if constexpr (F8) { _Pragma("unroll") for (int m = 0; m < 4; ++m) dst##8[m] = PG8_LD32(lds + PG8_SA(b, h) + aoff + m * 2048); } else { \
;         _Pragma("unroll") for (int m = 0; m < 4; ++m) _Pragma("unroll") for (int k = 0; k < 2; ++k) dst[m][k] = *(const LAS bf16x8*)(lds + PG8_SA(b, h) + aoff + m * 2048 + k * 1024); } } while (0)
; #define PG8_LDB(dst, b, h) do { if constexpr (F8) { _Pragma("unroll") for (int n = 0; n < 2; ++n) dst##8[n] = PG8_LD32(lds + PG8_SB(b, h) + boff + n * 2048); } else { \
;         _Pragma("unroll") for (int n = 0; n < 2; ++n) _Pragma("unroll") for (int k = 0; k < 2; ++k) dst[n][k] = *(const LAS bf16x8*)(lds + PG8_SB(b, h) + boff + n * 2048 + k * 1024); } } while (0)
; #define PG8_WAIT_VR() PG8_WAIT_V(8)
; #define PG8_WAIT_VX() do { if (relax) asm volatile("s_waitcnt vmcnt(%0)" :: "n"(8 + Epi::RELAX) : "memory"); else PG8_WAIT_V(8); } while (0)
; template <class Epi, class Sched, bool F8 = false, bool PF = false, bool I8 = false, int PID = -1>
; __device__ __forceinline__ void gemm_phase(LAS unsigned char* lds, LAS unsigned char* xlds, const int RP, const int RPB, const int nt, const Sched& S, const Epi& E, const int stagger_ticks) {
;     ...
;             PG8_WAIT_VX(); PG8_WAIT_L(0); PG8_BAR; PG8_MMA(1, 0, At, B0); PG8_MMA(1, 1, At, B1); PG8_BAR; PG8_SCHED;
;             PG8_LDB(B0, 1, 0); PG8_LDB(B1, 1, 1); PG8_SCHED; PG8_LDA(At, 1, 0); PG8_STAGEA1(PG8_SA(0, 1), a2);
;             PG8_WAIT_VR(); PG8_WAIT_L(0); PG8_BAR; PG8_MMA(0, 0, At, B0); PG8_MMA(0, 1, At, B1); PG8_BAR; PG8_SCHED;
;             PG8_LDA(At, 1, 1); PG8_STAGE(PG8_SB(1, 0), b3, voffB); PG8_STAGE(PG8_SB(1, 1), b3 + hstepB, voffB); PG8_STAGEA(PG8_SA(1, 0), a3, vA0, vA1);
;             PG8_WAIT_VR(); PG8_WAIT_L(0); PG8_BAR; PG8_MMA(1, 0, At, B0); PG8_MMA(1, 1, At, B1); PG8_BAR; PG8_SCHED;
;         }
	v_add_u32_e32 v14, 0x18000, v168
	v_add_u32_e32 v30, 0x1c000, v168
	ds_read_b128 v[2:5], v14
	ds_read_b128 v[6:9], v14 offset:1024
	ds_read_b128 v[10:13], v14 offset:2048
	ds_read_b128 v[14:17], v14 offset:3072
	ds_read_b128 v[18:21], v30
	ds_read_b128 v[22:25], v30 offset:1024
	ds_read_b128 v[26:29], v30 offset:2048
	ds_read_b128 v[30:33], v30 offset:3072
	ds_read_b128 v[34:37], v169 offset:32768
	ds_read_b128 v[38:41], v169 offset:33792
	ds_read_b128 v[42:45], v169 offset:34816
	ds_read_b128 v[46:49], v169 offset:35840
	ds_read_b128 v[50:53], v169 offset:36864
	ds_read_b128 v[54:57], v169 offset:37888
	ds_read_b128 v[58:61], v169 offset:38912
	ds_read_b128 v[62:65], v169 offset:39936
	s_add_u32 s38, s38, 0x20000
	s_addc_u32 s39, s39, 0
	s_add_i32 s75, s74, 0x4000
	s_mov_b32 m0, s75
	s_nop 0
	global_load_lds_dwordx4 v164, s[38:39]
	s_add_i32 s75, s74, 0x6000
	s_mov_b32 m0, s75
	s_nop 0
	global_load_lds_dwordx4 v165, s[38:39]
	s_waitcnt vmcnt(8)
	s_waitcnt lgkmcnt(0)
	s_barrier
	s_setprio 1
	s_waitcnt lgkmcnt(6)
	v_mfma_f32_16x16x128_f8f6f4 v[150:153], v[2:9], v[34:41], v[150:153]
	v_mfma_f32_16x16x128_f8f6f4 v[146:149], v[10:17], v[34:41], v[146:149]
	s_waitcnt lgkmcnt(4)
	v_mfma_f32_16x16x128_f8f6f4 v[134:137], v[2:9], v[42:49], v[134:137]
	v_mfma_f32_16x16x128_f8f6f4 v[130:133], v[10:17], v[42:49], v[130:133]
	s_waitcnt lgkmcnt(2)
	v_mfma_f32_16x16x128_f8f6f4 v[118:121], v[2:9], v[50:57], v[118:121]
	v_mfma_f32_16x16x128_f8f6f4 v[114:117], v[10:17], v[50:57], v[114:117]
	s_waitcnt lgkmcnt(0)
	v_mfma_f32_16x16x128_f8f6f4 v[102:105], v[2:9], v[58:65], v[102:105]
	v_mfma_f32_16x16x128_f8f6f4 v[98:101], v[10:17], v[58:65], v[98:101]
	s_setprio 0
	s_setprio 1
	v_mfma_f32_16x16x128_f8f6f4 v[158:161], v[18:25], v[34:41], v[158:161]
	v_mfma_f32_16x16x128_f8f6f4 v[154:157], v[26:33], v[34:41], v[154:157]
	v_mfma_f32_16x16x128_f8f6f4 v[142:145], v[18:25], v[42:49], v[142:145]
	v_mfma_f32_16x16x128_f8f6f4 v[138:141], v[26:33], v[42:49], v[138:141]
	v_mfma_f32_16x16x128_f8f6f4 v[126:129], v[18:25], v[50:57], v[126:129]
	v_mfma_f32_16x16x128_f8f6f4 v[122:125], v[26:33], v[50:57], v[122:125]
	v_mfma_f32_16x16x128_f8f6f4 v[110:113], v[18:25], v[58:65], v[110:113]
	v_mfma_f32_16x16x128_f8f6f4 v[106:109], v[26:33], v[58:65], v[106:109]
	s_setprio 0
	s_barrier
	ds_read_b128 v[42:45], v169 offset:49152
	ds_read_b128 v[46:49], v169 offset:50176
	ds_read_b128 v[58:61], v169 offset:51200
	ds_read_b128 v[62:65], v169 offset:52224
	ds_read_b128 v[170:173], v169 offset:53248
	ds_read_b128 v[174:177], v169 offset:54272
	ds_read_b128 v[178:181], v169 offset:55296
	ds_read_b128 v[182:185], v169 offset:56320
	s_add_i32 s38, s74, 0x18000
	s_mov_b32 m0, s38
	s_nop 0
	global_load_lds_dwordx4 v166, s[36:37]
	s_add_i32 s38, s74, 0x1a000
	s_mov_b32 m0, s38
	s_nop 0
	global_load_lds_dwordx4 v167, s[36:37]
	s_add_u32 s34, s34, 0x2080
	s_addc_u32 s35, s35, 0
	s_add_i32 s36, s74, 0x1c000
	s_mov_b32 m0, s36
	s_nop 0
	global_load_lds_dwordx4 v166, s[34:35]
	s_add_i32 s36, s74, 0x1e000
	s_mov_b32 m0, s36
	s_nop 0
	global_load_lds_dwordx4 v167, s[34:35]
	s_add_i32 s34, s74, 0x8000
	s_mov_b32 m0, s34
	s_nop 0
	global_load_lds_dwordx4 v164, s[30:31]
	s_add_i32 s74, s74, 0xa000
	s_mov_b32 m0, s74
	s_nop 0
	global_load_lds_dwordx4 v165, s[30:31]
	s_waitcnt vmcnt(8)
	s_waitcnt lgkmcnt(0)
	s_barrier
	s_setprio 1
	s_waitcnt lgkmcnt(6)
	v_mfma_f32_16x16x128_f8f6f4 v[86:89], v[2:9], v[42:49], v[86:89]
	v_mfma_f32_16x16x128_f8f6f4 v[82:85], v[10:17], v[42:49], v[82:85]
	s_waitcnt lgkmcnt(4)
	v_mfma_f32_16x16x128_f8f6f4 v[70:73], v[2:9], v[58:65], v[70:73]
	v_mfma_f32_16x16x128_f8f6f4 v[66:69], v[10:17], v[58:65], v[66:69]
	s_waitcnt lgkmcnt(2)
	v_mfma_f32_16x16x128_f8f6f4 v[54:57], v[2:9], v[170:177], v[202:205]
	v_mfma_f32_16x16x128_f8f6f4 v[50:53], v[10:17], v[170:177], v[206:209]
	s_waitcnt lgkmcnt(0)
	v_mfma_f32_16x16x128_f8f6f4 v[38:41], v[2:9], v[178:185], v[210:213]
	v_mfma_f32_16x16x128_f8f6f4 v[34:37], v[10:17], v[178:185], v[214:217]
	s_setprio 0
	s_setprio 1
	v_mfma_f32_16x16x128_f8f6f4 v[94:97], v[18:25], v[42:49], v[94:97]
	v_mfma_f32_16x16x128_f8f6f4 v[90:93], v[26:33], v[42:49], v[90:93]
	v_mfma_f32_16x16x128_f8f6f4 v[78:81], v[18:25], v[58:65], v[78:81]
	v_mfma_f32_16x16x128_f8f6f4 v[74:77], v[26:33], v[58:65], v[74:77]
	v_mfma_f32_16x16x128_f8f6f4 v[62:65], v[18:25], v[170:177], v[218:221]
	v_mfma_f32_16x16x128_f8f6f4 v[58:61], v[26:33], v[170:177], v[186:189]
	v_mfma_f32_16x16x128_f8f6f4 v[46:49], v[18:25], v[178:185], v[190:193]
	v_mfma_f32_16x16x128_f8f6f4 v[42:45], v[26:33], v[178:185], v[194:197]
	s_setprio 0
	s_barrier
	s_add_i32 s73, s73, 2
	s_add_u32 s25, s25, 0x100
	s_addc_u32 s71, s71, 0
	s_add_u32 s26, s26, 0x100
	s_addc_u32 s27, s27, 0
	s_cmp_gt_u32 s73, 5
	s_branch .LBB0_1063

; #define PG8_UNI64(p) ((const char*)((((unsigned long long)(unsigned)__builtin_amdgcn_readfirstlane((int)((unsigned long long)(p) >> 32))) << 32) | (unsigned long long)(unsigned)__builtin_amdgcn_readfirstlane((int)(unsigned)(unsigned long long)(p))))
; #define PG8_BAR __builtin_amdgcn_s_barrier()
;     __device__ __forceinline__ const char* Abase(const pg8::Unit& u) const { size_t o = WS_R1; if (u.aux == 1) o = WS_R3; return ws + o + (size_t)u.pm * TSF8; }
;     __device__ __forceinline__ const char* Bbase(const pg8::Unit& u) const { size_t o = WS_WIN; if (u.aux == 1) o = WS_WKV; return ws + o + (size_t)u.pn * TSF8; }
;     __device__ __forceinline__ const char* Abase(const pg8::Unit& u) const { if (GATH) return ws + WS_XQ; return ws + WS_H2 + (size_t)u.pm * TSF8; }
; template <class Epi, class Sched, bool F8 = false, bool PF = false, bool I8 = false, int PID = -1>
; __device__ __forceinline__ void gemm_phase(LAS unsigned char* lds, LAS unsigned char* xlds, const int RP, const int RPB, const int nt, const Sched& S, const Epi& E, const int stagger_ticks) {
;     ...
;         cur = nxt; cA = nA; cB = nB; ++ui;
;         has_next = has_nn; nxt = nn;
;         if (has_next) { nA = PG8_UNI64(S.Abase(nxt)); nB = PG8_UNI64(S.Bbase(nxt)); }
;         if (Sched::GATHER) { *nslot = (u32x4){gv[0], gv[1], gv[2], gv[3]}; asm volatile("" ::: "memory"); }
;         PG8_ZERO_ACC();
;         if (wr == 1) PG8_BAR;
.LBB0_1078:
	v_mov_b32_e32 v163, v162
	v_mov_b64_e32 v[2:3], v[162:163]
	s_andn2_b64 vcc, exec, s[16:17]
	s_cbranch_vccnz .LBB0_1059
	s_barrier
	s_branch .LBB0_1059
